# v14
# speedup vs baseline: 1.0411x; 1.0224x over previous
.LBB4_7:
	s_or_b64 exec, exec, s[4:5]
	v_lshlrev_b32_e32 v6, 2, v27
	s_waitcnt lgkmcnt(0)
	s_barrier
	ds_read_b32 v6, v6 offset:34816
	v_cvt_f32_f16_sdwa v9, v2 dst_sel:DWORD dst_unused:UNUSED_PAD src0_sel:WORD_1
	v_cvt_f32_f16_e32 v8, v2
	v_cvt_f32_f16_sdwa v11, v3 dst_sel:DWORD dst_unused:UNUSED_PAD src0_sel:WORD_1
	v_cvt_f32_f16_e32 v10, v3
	v_cvt_f32_f16_sdwa v13, v5 dst_sel:DWORD dst_unused:UNUSED_PAD src0_sel:WORD_1
	s_waitcnt lgkmcnt(0)
	v_pk_mul_f32 v[2:3], v[6:7], v[8:9] op_sel_hi:[0,1]
	v_cvt_f32_f16_e32 v12, v5
	v_pk_mul_f32 v[8:9], v[6:7], v[10:11] op_sel_hi:[0,1]
	v_cvt_f32_f16_sdwa v11, v4 dst_sel:DWORD dst_unused:UNUSED_PAD src0_sel:WORD_1
	v_cvt_f32_f16_e32 v10, v4
	s_movk_i32 s3, 0x600
	v_cvt_pk_f16_f32 v2, v2, v3
	v_cvt_pk_f16_f32 v3, v8, v9
	v_pk_mul_f32 v[4:5], v[6:7], v[10:11] op_sel_hi:[0,1]
	v_pk_mul_f32 v[6:7], v[6:7], v[12:13] op_sel_hi:[0,1]
	v_cvt_pk_f16_f32 v4, v4, v5
	v_cvt_pk_f16_f32 v5, v6, v7
	v_mov_b64_e32 v[6:7], s[6:7]
	v_mad_u64_u32 v[6:7], s[4:5], v28, s3, v[6:7]
	v_lshl_add_u64 v[6:7], s[8:9], 1, v[6:7]
	v_lshlrev_b32_e32 v8, 1, v30
	v_mov_b32_e32 v9, 0
	v_lshl_add_u64 v[6:7], v[6:7], 0, v[8:9]
	s_mov_b64 s[4:5], 0
	global_store_dwordx4 v[6:7], v[2:5], off sc1

.LBB4_20:
.LBB4_21:
	s_ashr_i32 s16, s46, 31
	s_mul_i32 s17, s46, s47
	s_mul_hi_u32 s18, s46, s7
	s_add_i32 s17, s18, s17
	s_mul_i32 s16, s16, s7
	s_add_i32 s17, s17, s16
	s_mul_i32 s16, s46, s7
	s_lshl_b64 s[16:17], s[16:17], 7
	s_add_u32 s46, s50, s16
	s_addc_u32 s47, s51, s17
	s_mul_hi_i32 s17, s61, s45
	s_mul_i32 s16, s61, s45
	s_lshl_b64 s[18:19], s[16:17], 2
	s_add_u32 s16, s20, s18
	s_addc_u32 s17, s21, s19
	s_add_u32 s18, s22, s18
	s_addc_u32 s19, s23, s19
	s_ashr_i32 s7, s6, 31
	s_lshl_b64 s[6:7], s[6:7], 1
	s_add_u32 s6, s46, s6
	s_addc_u32 s7, s47, s7
	s_waitcnt vmcnt(2)
	v_lshlrev_b32_e32 v18, 1, v38
	v_mov_b32_e32 v19, 0
	s_waitcnt vmcnt(1)
	v_lshl_add_u64 v[22:23], s[6:7], 0, v[18:19]
	ds_read_b128 v[18:21], v34
	v_or_b32_e32 v24, s60, v26
	v_mad_i64_i32 v[40:41], s[6:7], v24, s44, 0
	v_cndmask_b32_e64 v1, 0, 1, s[62:63]
	v_lshl_add_u64 v[40:41], v[40:41], 1, v[22:23]
	v_cmp_ne_u32_e64 s[6:7], 1, v1
	s_andn2_b64 vcc, exec, s[62:63]
	s_waitcnt lgkmcnt(0)
	global_store_dwordx4 v[40:41], v[18:21], off sc1
	s_cbranch_vccnz .LBB4_60
	v_fma_mix_f32 v1, v6, v18, 0 op_sel_hi:[0,1,0]
	v_fma_mix_f32 v1, v7, v18, v1 op_sel:[0,1,0] op_sel_hi:[0,1,0]
	v_fma_mix_f32 v1, v8, v19, v1 op_sel_hi:[0,1,0]
	s_waitcnt vmcnt(1)
	v_fma_mix_f32 v25, v14, v18, 0 op_sel_hi:[0,1,0]
	v_fma_mix_f32 v1, v9, v19, v1 op_sel:[0,1,0] op_sel_hi:[0,1,0]
	v_fma_mix_f32 v18, v15, v18, v25 op_sel:[0,1,0] op_sel_hi:[0,1,0]
	v_fma_mix_f32 v1, v2, v20, v1 op_sel_hi:[0,1,0]
	v_fma_mix_f32 v18, v16, v19, v18 op_sel_hi:[0,1,0]
	v_fma_mix_f32 v1, v3, v20, v1 op_sel:[0,1,0] op_sel_hi:[0,1,0]
	v_fma_mix_f32 v18, v17, v19, v18 op_sel:[0,1,0] op_sel_hi:[0,1,0]
	v_fma_mix_f32 v1, v4, v21, v1 op_sel_hi:[0,1,0]
	v_fma_mix_f32 v18, v10, v20, v18 op_sel_hi:[0,1,0]
	v_fma_mix_f32 v19, v5, v21, v1 op_sel:[0,1,0] op_sel_hi:[0,1,0]
	v_mbcnt_lo_u32_b32 v1, -1, 0
	v_fma_mix_f32 v18, v11, v20, v18 op_sel:[0,1,0] op_sel_hi:[0,1,0]
	v_mbcnt_hi_u32_b32 v20, -1, v1
	v_and_b32_e32 v1, 64, v20
	v_add_u32_e32 v25, 64, v1
	v_xor_b32_e32 v1, 1, v20
	v_cmp_lt_i32_e32 vcc, v1, v25
	v_fma_mix_f32 v18, v12, v21, v18 op_sel_hi:[0,1,0]
	v_fma_mix_f32 v18, v13, v21, v18 op_sel:[0,1,0] op_sel_hi:[0,1,0]
	v_cndmask_b32_e32 v1, v20, v1, vcc
	v_lshlrev_b32_e32 v1, 2, v1
	ds_bpermute_b32 v21, v1, v19
	ds_bpermute_b32 v27, v1, v18
	s_waitcnt lgkmcnt(1)
	v_add_f32_e32 v19, v19, v21
	s_waitcnt lgkmcnt(0)
	v_add_f32_e32 v21, v18, v27
	v_xor_b32_e32 v18, 2, v20
	v_cmp_lt_i32_e32 vcc, v18, v25
	s_nop 1
	v_cndmask_b32_e32 v18, v20, v18, vcc
	v_lshlrev_b32_e32 v18, 2, v18
	ds_bpermute_b32 v27, v18, v19
	ds_bpermute_b32 v39, v18, v21
	s_waitcnt lgkmcnt(1)
	v_add_f32_e32 v27, v19, v27
	v_xor_b32_e32 v19, 4, v20
	v_cmp_lt_i32_e32 vcc, v19, v25
	s_waitcnt lgkmcnt(0)
	v_add_f32_e32 v39, v21, v39
	v_cndmask_b32_e32 v19, v20, v19, vcc
	v_lshlrev_b32_e32 v19, 2, v19
	ds_bpermute_b32 v21, v19, v27
	ds_bpermute_b32 v40, v19, v39
	s_waitcnt lgkmcnt(1)
	v_add_f32_e32 v21, v27, v21
	s_waitcnt lgkmcnt(0)
	v_add_f32_e32 v27, v39, v40
	v_xor_b32_e32 v39, 8, v20
	v_cmp_lt_i32_e32 vcc, v39, v25
	v_ashrrev_i32_e32 v25, 31, v24
	s_nop 0
	v_cndmask_b32_e32 v20, v20, v39, vcc
	v_lshlrev_b32_e32 v20, 2, v20
	ds_bpermute_b32 v39, v20, v21
	ds_bpermute_b32 v40, v20, v27
	v_cmp_gt_i32_e32 vcc, s45, v24
	s_and_b64 s[22:23], s[4:5], vcc
	s_and_saveexec_b64 s[20:21], s[22:23]
	s_cbranch_execz .LBB4_24
	v_lshlrev_b64 v[24:25], 2, v[24:25]
	s_waitcnt lgkmcnt(0)
	v_add_f32_e32 v27, v27, v40
	v_add_f32_e32 v21, v21, v39
	v_lshl_add_u64 v[40:41], s[18:19], 0, v[24:25]
	v_lshl_add_u64 v[24:25], s[16:17], 0, v[24:25]
	global_store_dword v[24:25], v21, off sc1
	global_store_dword v[40:41], v27, off sc1
.LBB4_24:
	s_or_b64 exec, exec, s[20:21]
	s_waitcnt lgkmcnt(0)
	ds_read_b128 v[40:43], v33
	v_or_b32_e32 v27, s60, v30
	v_cmp_gt_i32_e32 vcc, s45, v27
	s_and_b64 s[22:23], s[4:5], vcc
	s_waitcnt lgkmcnt(0)
	v_fma_mix_f32 v21, v6, v40, 0 op_sel_hi:[0,1,0]
	v_fma_mix_f32 v24, v14, v40, 0 op_sel_hi:[0,1,0]
	v_fma_mix_f32 v21, v7, v40, v21 op_sel:[0,1,0] op_sel_hi:[0,1,0]
	v_fma_mix_f32 v24, v15, v40, v24 op_sel:[0,1,0] op_sel_hi:[0,1,0]
	v_fma_mix_f32 v21, v8, v41, v21 op_sel_hi:[0,1,0]
	v_fma_mix_f32 v24, v16, v41, v24 op_sel_hi:[0,1,0]
	v_fma_mix_f32 v21, v9, v41, v21 op_sel:[0,1,0] op_sel_hi:[0,1,0]
	v_fma_mix_f32 v24, v17, v41, v24 op_sel:[0,1,0] op_sel_hi:[0,1,0]
	v_fma_mix_f32 v21, v2, v42, v21 op_sel_hi:[0,1,0]
	v_fma_mix_f32 v24, v10, v42, v24 op_sel_hi:[0,1,0]
	v_fma_mix_f32 v21, v3, v42, v21 op_sel:[0,1,0] op_sel_hi:[0,1,0]
	v_fma_mix_f32 v24, v11, v42, v24 op_sel:[0,1,0] op_sel_hi:[0,1,0]
	v_fma_mix_f32 v21, v4, v43, v21 op_sel_hi:[0,1,0]
	v_fma_mix_f32 v24, v12, v43, v24 op_sel_hi:[0,1,0]
	v_fma_mix_f32 v21, v5, v43, v21 op_sel:[0,1,0] op_sel_hi:[0,1,0]
	v_fma_mix_f32 v24, v13, v43, v24 op_sel:[0,1,0] op_sel_hi:[0,1,0]
	ds_bpermute_b32 v25, v1, v21
	ds_bpermute_b32 v1, v1, v24
	s_waitcnt lgkmcnt(1)
	v_add_f32_e32 v21, v21, v25
	s_waitcnt lgkmcnt(0)
	v_add_f32_e32 v1, v24, v1
	ds_bpermute_b32 v24, v18, v21
	ds_bpermute_b32 v18, v18, v1
	s_waitcnt lgkmcnt(1)
	v_add_f32_e32 v21, v21, v24
	s_waitcnt lgkmcnt(0)
	v_add_f32_e32 v18, v1, v18
	ds_bpermute_b32 v1, v19, v21
	ds_bpermute_b32 v19, v19, v18
	v_mad_i64_i32 v[24:25], s[20:21], v27, s44, 0
	v_lshl_add_u64 v[24:25], v[24:25], 1, v[22:23]
	s_waitcnt lgkmcnt(1)
	v_add_f32_e32 v1, v21, v1
	s_waitcnt lgkmcnt(0)
	v_add_f32_e32 v18, v18, v19
	ds_bpermute_b32 v19, v20, v1
	ds_bpermute_b32 v20, v20, v18
	global_store_dwordx4 v[24:25], v[40:43], off sc1
	s_and_saveexec_b64 s[20:21], s[22:23]
	s_cbranch_execz .LBB4_26
	s_ashr_i32 s61, s60, 31
	v_mov_b32_e32 v27, 0
	s_waitcnt lgkmcnt(0)
	v_add_f32_e32 v24, v18, v20
	v_add_f32_e32 v1, v1, v19
	v_lshl_add_u64 v[18:19], s[60:61], 0, v[26:27]
	v_lshlrev_b64 v[18:19], 2, v[18:19]
	v_lshl_add_u64 v[20:21], s[18:19], 0, v[18:19]
	v_lshl_add_u64 v[18:19], s[16:17], 0, v[18:19]
	global_store_dword v[18:19], v1, off offset:64 sc1
	global_store_dword v[20:21], v24, off offset:64 sc1

.LBB4_27:
	s_waitcnt lgkmcnt(0)
	ds_read_b128 v[18:21], v33
	v_or_b32_e32 v1, s60, v30
	v_mad_i64_i32 v[24:25], s[20:21], v1, s44, 0
	v_lshl_add_u64 v[24:25], v[24:25], 1, v[22:23]
	s_waitcnt lgkmcnt(0)
	global_store_dwordx4 v[24:25], v[18:21], off sc1
.LBB4_28:
	s_waitcnt lgkmcnt(0)
	ds_read_b128 v[18:21], v32
	v_or_b32_e32 v24, s60, v29
	v_mad_i64_i32 v[40:41], s[20:21], v24, s44, 0
	v_lshl_add_u64 v[40:41], v[40:41], 1, v[22:23]
	s_and_b64 vcc, exec, s[6:7]
	s_waitcnt lgkmcnt(0)
	global_store_dwordx4 v[40:41], v[18:21], off sc1
	s_cbranch_vccnz .LBB4_61
	v_fma_mix_f32 v1, v6, v18, 0 op_sel_hi:[0,1,0]
	v_fma_mix_f32 v1, v7, v18, v1 op_sel:[0,1,0] op_sel_hi:[0,1,0]
	v_fma_mix_f32 v1, v8, v19, v1 op_sel_hi:[0,1,0]
	s_waitcnt vmcnt(2)
	v_fma_mix_f32 v25, v14, v18, 0 op_sel_hi:[0,1,0]
	v_fma_mix_f32 v1, v9, v19, v1 op_sel:[0,1,0] op_sel_hi:[0,1,0]
	v_fma_mix_f32 v18, v15, v18, v25 op_sel:[0,1,0] op_sel_hi:[0,1,0]
	v_fma_mix_f32 v1, v2, v20, v1 op_sel_hi:[0,1,0]
	v_fma_mix_f32 v18, v16, v19, v18 op_sel_hi:[0,1,0]
	v_fma_mix_f32 v1, v3, v20, v1 op_sel:[0,1,0] op_sel_hi:[0,1,0]
	v_fma_mix_f32 v18, v17, v19, v18 op_sel:[0,1,0] op_sel_hi:[0,1,0]
	v_fma_mix_f32 v1, v4, v21, v1 op_sel_hi:[0,1,0]
	v_fma_mix_f32 v18, v10, v20, v18 op_sel_hi:[0,1,0]
	v_fma_mix_f32 v19, v5, v21, v1 op_sel:[0,1,0] op_sel_hi:[0,1,0]
	v_mbcnt_lo_u32_b32 v1, -1, 0
	v_fma_mix_f32 v18, v11, v20, v18 op_sel:[0,1,0] op_sel_hi:[0,1,0]
	v_mbcnt_hi_u32_b32 v20, -1, v1
	v_and_b32_e32 v1, 64, v20
	v_add_u32_e32 v27, 64, v1
	v_xor_b32_e32 v1, 1, v20
	v_cmp_lt_i32_e32 vcc, v1, v27
	v_fma_mix_f32 v18, v12, v21, v18 op_sel_hi:[0,1,0]
	v_fma_mix_f32 v18, v13, v21, v18 op_sel:[0,1,0] op_sel_hi:[0,1,0]
	v_cndmask_b32_e32 v1, v20, v1, vcc
	v_lshlrev_b32_e32 v1, 2, v1
	ds_bpermute_b32 v21, v1, v19
	ds_bpermute_b32 v25, v1, v18
	s_waitcnt lgkmcnt(1)
	v_add_f32_e32 v19, v19, v21
	s_waitcnt lgkmcnt(0)
	v_add_f32_e32 v21, v18, v25
	v_xor_b32_e32 v18, 2, v20
	v_cmp_lt_i32_e32 vcc, v18, v27
	s_nop 1
	v_cndmask_b32_e32 v18, v20, v18, vcc
	v_lshlrev_b32_e32 v18, 2, v18
	ds_bpermute_b32 v25, v18, v19
	ds_bpermute_b32 v39, v18, v21
	s_waitcnt lgkmcnt(1)
	v_add_f32_e32 v25, v19, v25
	v_xor_b32_e32 v19, 4, v20
	v_cmp_lt_i32_e32 vcc, v19, v27
	s_waitcnt lgkmcnt(0)
	v_add_f32_e32 v39, v21, v39
	v_cndmask_b32_e32 v19, v20, v19, vcc
	v_lshlrev_b32_e32 v19, 2, v19
	ds_bpermute_b32 v21, v19, v25
	ds_bpermute_b32 v40, v19, v39
	s_waitcnt lgkmcnt(1)
	v_add_f32_e32 v21, v25, v21
	s_waitcnt lgkmcnt(0)
	v_add_f32_e32 v25, v39, v40
	v_xor_b32_e32 v39, 8, v20
	v_cmp_lt_i32_e32 vcc, v39, v27
	s_nop 1
	v_cndmask_b32_e32 v20, v20, v39, vcc
	v_lshlrev_b32_e32 v20, 2, v20
	ds_bpermute_b32 v27, v20, v21
	ds_bpermute_b32 v39, v20, v25
	v_cmp_gt_i32_e32 vcc, s45, v24
	s_and_b64 s[20:21], s[4:5], vcc
	s_and_saveexec_b64 s[6:7], s[20:21]
	s_cbranch_execz .LBB4_31
	s_waitcnt lgkmcnt(1)
	v_add_f32_e32 v21, v21, v27
	s_ashr_i32 s61, s60, 31
	v_mov_b32_e32 v27, 0
	s_waitcnt lgkmcnt(0)
	v_add_f32_e32 v39, v25, v39
	v_lshl_add_u64 v[24:25], s[60:61], 0, v[26:27]
	v_lshlrev_b64 v[24:25], 2, v[24:25]
	v_lshl_add_u64 v[40:41], s[18:19], 0, v[24:25]
	v_lshl_add_u64 v[24:25], s[16:17], 0, v[24:25]
	global_store_dword v[24:25], v21, off offset:128 sc1
	global_store_dword v[40:41], v39, off offset:128 sc1
.LBB4_31:
	s_or_b64 exec, exec, s[6:7]
	ds_read_b128 v[40:43], v31
	s_waitcnt lgkmcnt(0)
	v_fma_mix_f32 v6, v6, v40, 0 op_sel_hi:[0,1,0]
	v_fma_mix_f32 v14, v14, v40, 0 op_sel_hi:[0,1,0]
	v_fma_mix_f32 v6, v7, v40, v6 op_sel:[0,1,0] op_sel_hi:[0,1,0]
	v_fma_mix_f32 v7, v15, v40, v14 op_sel:[0,1,0] op_sel_hi:[0,1,0]
	v_fma_mix_f32 v6, v8, v41, v6 op_sel_hi:[0,1,0]
	v_fma_mix_f32 v7, v16, v41, v7 op_sel_hi:[0,1,0]
	v_fma_mix_f32 v6, v9, v41, v6 op_sel:[0,1,0] op_sel_hi:[0,1,0]
	v_fma_mix_f32 v7, v17, v41, v7 op_sel:[0,1,0] op_sel_hi:[0,1,0]
	v_fma_mix_f32 v2, v2, v42, v6 op_sel_hi:[0,1,0]
	v_fma_mix_f32 v6, v10, v42, v7 op_sel_hi:[0,1,0]
	v_fma_mix_f32 v2, v3, v42, v2 op_sel:[0,1,0] op_sel_hi:[0,1,0]
	v_fma_mix_f32 v3, v11, v42, v6 op_sel:[0,1,0] op_sel_hi:[0,1,0]
	v_fma_mix_f32 v2, v4, v43, v2 op_sel_hi:[0,1,0]
	v_fma_mix_f32 v3, v12, v43, v3 op_sel_hi:[0,1,0]
	v_fma_mix_f32 v2, v5, v43, v2 op_sel:[0,1,0] op_sel_hi:[0,1,0]
	v_fma_mix_f32 v3, v13, v43, v3 op_sel:[0,1,0] op_sel_hi:[0,1,0]
	ds_bpermute_b32 v4, v1, v2
	ds_bpermute_b32 v1, v1, v3
	v_or_b32_e32 v5, s60, v28
	v_mad_i64_i32 v[6:7], s[6:7], v5, s44, 0
	s_waitcnt lgkmcnt(1)
	v_add_f32_e32 v2, v2, v4
	s_waitcnt lgkmcnt(0)
	v_add_f32_e32 v1, v3, v1
	ds_bpermute_b32 v3, v18, v2
	ds_bpermute_b32 v4, v18, v1
	v_cmp_gt_i32_e32 vcc, s45, v5
	v_lshl_add_u64 v[6:7], v[6:7], 1, v[22:23]
	s_and_b64 s[20:21], s[4:5], vcc
	s_waitcnt lgkmcnt(1)
	v_add_f32_e32 v2, v2, v3
	s_waitcnt lgkmcnt(0)
	v_add_f32_e32 v3, v1, v4
	ds_bpermute_b32 v1, v19, v2
	ds_bpermute_b32 v4, v19, v3
	global_store_dwordx4 v[6:7], v[40:43], off sc1
	s_waitcnt lgkmcnt(1)
	v_add_f32_e32 v1, v2, v1
	s_waitcnt lgkmcnt(0)
	v_add_f32_e32 v2, v3, v4
	ds_bpermute_b32 v3, v20, v1
	ds_bpermute_b32 v4, v20, v2
	s_and_saveexec_b64 s[6:7], s[20:21]
	s_cbranch_execz .LBB4_33
	s_ashr_i32 s61, s60, 31
	v_mov_b32_e32 v27, 0
	s_waitcnt lgkmcnt(0)
	v_add_f32_e32 v6, v2, v4
	v_add_f32_e32 v1, v1, v3
	v_lshl_add_u64 v[2:3], s[60:61], 0, v[26:27]
	v_lshlrev_b64 v[2:3], 2, v[2:3]
	v_lshl_add_u64 v[4:5], s[18:19], 0, v[2:3]
	v_lshl_add_u64 v[2:3], s[16:17], 0, v[2:3]
	global_store_dword v[2:3], v1, off offset:192 sc1
	global_store_dword v[4:5], v6, off offset:192 sc1

.LBB4_34:
	s_waitcnt lgkmcnt(0)
	ds_read_b128 v[2:5], v31
	v_or_b32_e32 v1, s60, v28
	v_mad_i64_i32 v[6:7], s[6:7], v1, s44, 0
	v_lshl_add_u64 v[6:7], v[6:7], 1, v[22:23]
	s_waitcnt lgkmcnt(0)
	global_store_dwordx4 v[6:7], v[2:5], off sc1

.LBB4_46:
	s_or_b64 exec, exec, s[56:57]
	s_waitcnt lgkmcnt(0)
	s_barrier
	s_and_saveexec_b64 s[48:49], s[2:3]
	s_cbranch_execz .LBB4_48
	s_ashr_i32 s41, s42, 31
	s_mul_i32 s43, s42, s43
	s_mul_hi_u32 s56, s42, s7
	s_add_i32 s43, s56, s43
	s_mul_i32 s41, s41, s7
	s_add_i32 s43, s43, s41
	s_mul_i32 s42, s42, s7
	s_lshl_b64 s[42:43], s[42:43], 7
	s_add_u32 s41, s50, s42
	s_addc_u32 s42, s51, s43
	s_ashr_i32 s7, s6, 31
	s_lshl_b64 s[6:7], s[6:7], 1
	s_add_u32 s6, s41, s6
	s_addc_u32 s7, s42, s7
	v_lshlrev_b32_e32 v0, 1, v24
	v_mov_b32_e32 v1, 0
	v_lshl_add_u64 v[8:9], s[6:7], 0, v[0:1]
	ds_read_b128 v[0:3], v34
	v_or_b32_e32 v4, s33, v26
	v_mad_i64_i32 v[4:5], s[6:7], v4, s40, 0
	v_lshl_add_u64 v[10:11], v[4:5], 1, v[8:9]
	ds_read_b128 v[4:7], v33
	s_waitcnt lgkmcnt(1)
	global_store_dwordx4 v[10:11], v[0:3], off sc1
	s_nop 1
	v_or_b32_e32 v0, s33, v30
	v_mad_i64_i32 v[0:1], s[6:7], v0, s40, 0
	v_lshl_add_u64 v[0:1], v[0:1], 1, v[8:9]
	s_waitcnt lgkmcnt(0)
	global_store_dwordx4 v[0:1], v[4:7], off sc1
	ds_read_b128 v[0:3], v32
	s_nop 0
	v_or_b32_e32 v4, s33, v29
	v_mad_i64_i32 v[4:5], s[6:7], v4, s40, 0
	v_lshl_add_u64 v[10:11], v[4:5], 1, v[8:9]
	ds_read_b128 v[4:7], v31
	s_waitcnt lgkmcnt(1)
	global_store_dwordx4 v[10:11], v[0:3], off sc1
	s_nop 1
	v_or_b32_e32 v0, s33, v28
	v_mad_i64_i32 v[0:1], s[6:7], v0, s40, 0
	v_lshl_add_u64 v[0:1], v[0:1], 1, v[8:9]
	s_waitcnt lgkmcnt(0)
	global_store_dwordx4 v[0:1], v[4:7], off sc1

.LBB4_62:
.LBB4_63:
	s_ashr_i32 s8, s38, 31
	s_mul_i32 s9, s38, s41
	s_mul_hi_u32 s10, s38, s39
	s_add_i32 s9, s10, s9
	s_mul_i32 s8, s8, s39
	s_add_i32 s9, s9, s8
	s_mul_i32 s8, s38, s39
	s_lshl_b64 s[8:9], s[8:9], 7
	s_add_u32 s38, s46, s8
	s_addc_u32 s39, s47, s9
	s_mul_hi_i32 s9, s1, s37
	s_mul_i32 s8, s1, s37
	s_lshl_b64 s[10:11], s[8:9], 2
	s_add_u32 s8, s12, s10
	s_addc_u32 s9, s13, s11
	s_add_u32 s10, s14, s10
	s_addc_u32 s11, s15, s11
	s_ashr_i32 s1, s0, 31
	s_lshl_b64 s[0:1], s[0:1], 1
	s_add_u32 s0, s38, s0
	s_addc_u32 s1, s39, s1
	v_lshlrev_b32_e32 v16, 1, v38
	v_mov_b32_e32 v17, 0
	v_lshl_add_u64 v[20:21], s[0:1], 0, v[16:17]
	ds_read_b128 v[16:19], v34
	v_or_b32_e32 v22, s40, v26
	v_mad_i64_i32 v[38:39], s[0:1], v22, s36, 0
	v_cndmask_b32_e64 v23, 0, 1, s[44:45]
	v_lshl_add_u64 v[38:39], v[38:39], 1, v[20:21]
	v_cmp_ne_u32_e64 s[0:1], 1, v23
	s_andn2_b64 vcc, exec, s[44:45]
	v_mbcnt_lo_u32_b32 v25, -1, 0
	s_waitcnt lgkmcnt(0)
	global_store_dwordx4 v[38:39], v[16:19], off sc1
	s_cbranch_vccnz .LBB4_69
	s_waitcnt vmcnt(3)
	v_fma_mix_f32 v23, v4, v16, 0 op_sel_hi:[0,1,0]
	s_waitcnt vmcnt(1)
	v_fma_mix_f32 v27, v12, v16, 0 op_sel_hi:[0,1,0]
	v_fma_mix_f32 v23, v5, v16, v23 op_sel:[0,1,0] op_sel_hi:[0,1,0]
	v_fma_mix_f32 v16, v13, v16, v27 op_sel:[0,1,0] op_sel_hi:[0,1,0]
	v_fma_mix_f32 v23, v6, v17, v23 op_sel_hi:[0,1,0]
	v_fma_mix_f32 v16, v14, v17, v16 op_sel_hi:[0,1,0]
	v_fma_mix_f32 v23, v7, v17, v23 op_sel:[0,1,0] op_sel_hi:[0,1,0]
	v_fma_mix_f32 v16, v15, v17, v16 op_sel:[0,1,0] op_sel_hi:[0,1,0]
	v_fma_mix_f32 v17, v0, v18, v23 op_sel_hi:[0,1,0]
	v_fma_mix_f32 v16, v8, v18, v16 op_sel_hi:[0,1,0]
	v_fma_mix_f32 v17, v1, v18, v17 op_sel:[0,1,0] op_sel_hi:[0,1,0]
	v_fma_mix_f32 v16, v9, v18, v16 op_sel:[0,1,0] op_sel_hi:[0,1,0]
	v_fma_mix_f32 v17, v2, v19, v17 op_sel_hi:[0,1,0]
	v_fma_mix_f32 v16, v10, v19, v16 op_sel_hi:[0,1,0]
	v_fma_mix_f32 v17, v3, v19, v17 op_sel:[0,1,0] op_sel_hi:[0,1,0]
	v_fma_mix_f32 v18, v11, v19, v16 op_sel:[0,1,0] op_sel_hi:[0,1,0]
	v_mbcnt_hi_u32_b32 v19, -1, v25
	v_and_b32_e32 v16, 64, v19
	v_add_u32_e32 v23, 64, v16
	v_xor_b32_e32 v16, 1, v19
	v_cmp_lt_i32_e32 vcc, v16, v23
	s_nop 1
	v_cndmask_b32_e32 v16, v19, v16, vcc
	v_lshlrev_b32_e32 v16, 2, v16
	ds_bpermute_b32 v27, v16, v17
	ds_bpermute_b32 v38, v16, v18
	s_waitcnt lgkmcnt(1)
	v_add_f32_e32 v27, v17, v27
	v_xor_b32_e32 v17, 2, v19
	v_cmp_lt_i32_e32 vcc, v17, v23
	s_waitcnt lgkmcnt(0)
	v_add_f32_e32 v18, v18, v38
	v_cndmask_b32_e32 v17, v19, v17, vcc
	v_lshlrev_b32_e32 v17, 2, v17
	ds_bpermute_b32 v38, v17, v27
	ds_bpermute_b32 v39, v17, v18
	s_waitcnt lgkmcnt(1)
	v_add_f32_e32 v27, v27, v38
	s_waitcnt lgkmcnt(0)
	v_add_f32_e32 v38, v18, v39
	v_xor_b32_e32 v18, 4, v19
	v_cmp_lt_i32_e32 vcc, v18, v23
	s_nop 1
	v_cndmask_b32_e32 v18, v19, v18, vcc
	v_lshlrev_b32_e32 v18, 2, v18
	ds_bpermute_b32 v39, v18, v27
	ds_bpermute_b32 v40, v18, v38
	s_waitcnt lgkmcnt(1)
	v_add_f32_e32 v27, v27, v39
	v_xor_b32_e32 v39, 8, v19
	v_cmp_lt_i32_e32 vcc, v39, v23
	s_waitcnt lgkmcnt(0)
	v_add_f32_e32 v38, v38, v40
	v_ashrrev_i32_e32 v23, 31, v22
	v_cndmask_b32_e32 v19, v19, v39, vcc
	v_lshlrev_b32_e32 v19, 2, v19
	ds_bpermute_b32 v39, v19, v27
	ds_bpermute_b32 v40, v19, v38
	v_cmp_gt_i32_e32 vcc, s37, v22
	s_and_b64 s[14:15], s[4:5], vcc
	s_and_saveexec_b64 s[12:13], s[14:15]
	s_cbranch_execz .LBB4_66
	v_lshlrev_b64 v[22:23], 2, v[22:23]
	s_waitcnt lgkmcnt(0)
	v_add_f32_e32 v40, v38, v40
	v_add_f32_e32 v27, v27, v39
	v_lshl_add_u64 v[38:39], s[10:11], 0, v[22:23]
	v_lshl_add_u64 v[22:23], s[8:9], 0, v[22:23]
	global_store_dword v[22:23], v27, off sc1
	global_store_dword v[38:39], v40, off sc1
.LBB4_66:
	s_or_b64 exec, exec, s[12:13]
	s_waitcnt lgkmcnt(0)
	ds_read_b128 v[38:41], v33
	v_or_b32_e32 v42, s40, v30
	v_cmp_gt_i32_e32 vcc, s37, v42
	s_and_b64 s[14:15], s[4:5], vcc
	s_waitcnt lgkmcnt(0)
	v_fma_mix_f32 v22, v4, v38, 0 op_sel_hi:[0,1,0]
	v_fma_mix_f32 v23, v12, v38, 0 op_sel_hi:[0,1,0]
	v_fma_mix_f32 v22, v5, v38, v22 op_sel:[0,1,0] op_sel_hi:[0,1,0]
	v_fma_mix_f32 v23, v13, v38, v23 op_sel:[0,1,0] op_sel_hi:[0,1,0]
	v_fma_mix_f32 v22, v6, v39, v22 op_sel_hi:[0,1,0]
	v_fma_mix_f32 v23, v14, v39, v23 op_sel_hi:[0,1,0]
	v_fma_mix_f32 v22, v7, v39, v22 op_sel:[0,1,0] op_sel_hi:[0,1,0]
	v_fma_mix_f32 v23, v15, v39, v23 op_sel:[0,1,0] op_sel_hi:[0,1,0]
	v_fma_mix_f32 v22, v0, v40, v22 op_sel_hi:[0,1,0]
	v_fma_mix_f32 v23, v8, v40, v23 op_sel_hi:[0,1,0]
	v_fma_mix_f32 v22, v1, v40, v22 op_sel:[0,1,0] op_sel_hi:[0,1,0]
	v_fma_mix_f32 v23, v9, v40, v23 op_sel:[0,1,0] op_sel_hi:[0,1,0]
	v_fma_mix_f32 v22, v2, v41, v22 op_sel_hi:[0,1,0]
	v_fma_mix_f32 v23, v10, v41, v23 op_sel_hi:[0,1,0]
	v_fma_mix_f32 v22, v3, v41, v22 op_sel:[0,1,0] op_sel_hi:[0,1,0]
	v_fma_mix_f32 v23, v11, v41, v23 op_sel:[0,1,0] op_sel_hi:[0,1,0]
	ds_bpermute_b32 v27, v16, v22
	ds_bpermute_b32 v16, v16, v23
	s_waitcnt lgkmcnt(1)
	v_add_f32_e32 v22, v22, v27
	s_waitcnt lgkmcnt(0)
	v_add_f32_e32 v16, v23, v16
	ds_bpermute_b32 v23, v17, v22
	ds_bpermute_b32 v17, v17, v16
	s_waitcnt lgkmcnt(1)
	v_add_f32_e32 v27, v22, v23
	s_waitcnt lgkmcnt(0)
	v_add_f32_e32 v17, v16, v17
	ds_bpermute_b32 v16, v18, v27
	ds_bpermute_b32 v18, v18, v17
	v_mad_i64_i32 v[22:23], s[12:13], v42, s36, 0
	v_lshl_add_u64 v[22:23], v[22:23], 1, v[20:21]
	s_waitcnt lgkmcnt(1)
	v_add_f32_e32 v16, v27, v16
	s_waitcnt lgkmcnt(0)
	v_add_f32_e32 v17, v17, v18
	ds_bpermute_b32 v18, v19, v16
	ds_bpermute_b32 v19, v19, v17
	global_store_dwordx4 v[22:23], v[38:41], off sc1
	s_and_saveexec_b64 s[12:13], s[14:15]
	s_cbranch_execz .LBB4_68
	s_ashr_i32 s41, s40, 31
	v_mov_b32_e32 v27, 0
	s_waitcnt lgkmcnt(0)
	v_add_f32_e32 v22, v17, v19
	v_add_f32_e32 v23, v16, v18
	v_lshl_add_u64 v[16:17], s[40:41], 0, v[26:27]
	v_lshlrev_b64 v[16:17], 2, v[16:17]
	v_lshl_add_u64 v[18:19], s[10:11], 0, v[16:17]
	v_lshl_add_u64 v[16:17], s[8:9], 0, v[16:17]
	global_store_dword v[16:17], v23, off offset:64 sc1
	global_store_dword v[18:19], v22, off offset:64 sc1

.LBB4_70:
	s_and_b64 vcc, exec, s[12:13]
	s_cbranch_vccz .LBB4_72
	s_waitcnt lgkmcnt(0)
	ds_read_b128 v[16:19], v33
	v_or_b32_e32 v22, s40, v30
	v_mad_i64_i32 v[22:23], s[12:13], v22, s36, 0
	v_lshl_add_u64 v[22:23], v[22:23], 1, v[20:21]
	s_waitcnt lgkmcnt(0)
	global_store_dwordx4 v[22:23], v[16:19], off sc1
.LBB4_72:
	s_waitcnt lgkmcnt(0)
	ds_read_b128 v[16:19], v32
	v_or_b32_e32 v22, s40, v29
	v_mad_i64_i32 v[38:39], s[12:13], v22, s36, 0
	v_lshl_add_u64 v[38:39], v[38:39], 1, v[20:21]
	s_and_b64 vcc, exec, s[0:1]
	s_waitcnt lgkmcnt(0)
	global_store_dwordx4 v[38:39], v[16:19], off sc1
	s_cbranch_vccnz .LBB4_78
	s_waitcnt vmcnt(4)
	v_fma_mix_f32 v23, v4, v16, 0 op_sel_hi:[0,1,0]
	s_waitcnt vmcnt(2)
	v_fma_mix_f32 v27, v12, v16, 0 op_sel_hi:[0,1,0]
	v_fma_mix_f32 v23, v5, v16, v23 op_sel:[0,1,0] op_sel_hi:[0,1,0]
	v_fma_mix_f32 v16, v13, v16, v27 op_sel:[0,1,0] op_sel_hi:[0,1,0]
	v_fma_mix_f32 v23, v6, v17, v23 op_sel_hi:[0,1,0]
	v_fma_mix_f32 v16, v14, v17, v16 op_sel_hi:[0,1,0]
	v_fma_mix_f32 v23, v7, v17, v23 op_sel:[0,1,0] op_sel_hi:[0,1,0]
	v_fma_mix_f32 v16, v15, v17, v16 op_sel:[0,1,0] op_sel_hi:[0,1,0]
	v_fma_mix_f32 v17, v0, v18, v23 op_sel_hi:[0,1,0]
	v_fma_mix_f32 v16, v8, v18, v16 op_sel_hi:[0,1,0]
	v_fma_mix_f32 v17, v1, v18, v17 op_sel:[0,1,0] op_sel_hi:[0,1,0]
	v_fma_mix_f32 v16, v9, v18, v16 op_sel:[0,1,0] op_sel_hi:[0,1,0]
	v_fma_mix_f32 v17, v2, v19, v17 op_sel_hi:[0,1,0]
	v_fma_mix_f32 v16, v10, v19, v16 op_sel_hi:[0,1,0]
	v_fma_mix_f32 v17, v3, v19, v17 op_sel:[0,1,0] op_sel_hi:[0,1,0]
	v_fma_mix_f32 v18, v11, v19, v16 op_sel:[0,1,0] op_sel_hi:[0,1,0]
	v_mbcnt_hi_u32_b32 v19, -1, v25
	v_and_b32_e32 v16, 64, v19
	v_add_u32_e32 v27, 64, v16
	v_xor_b32_e32 v16, 1, v19
	v_cmp_lt_i32_e32 vcc, v16, v27
	s_nop 1
	v_cndmask_b32_e32 v16, v19, v16, vcc
	v_lshlrev_b32_e32 v16, 2, v16
	ds_bpermute_b32 v23, v16, v17
	ds_bpermute_b32 v25, v16, v18
	s_waitcnt lgkmcnt(1)
	v_add_f32_e32 v23, v17, v23
	v_xor_b32_e32 v17, 2, v19
	v_cmp_lt_i32_e32 vcc, v17, v27
	s_waitcnt lgkmcnt(0)
	v_add_f32_e32 v18, v18, v25
	v_cndmask_b32_e32 v17, v19, v17, vcc
	v_lshlrev_b32_e32 v17, 2, v17
	ds_bpermute_b32 v25, v17, v23
	ds_bpermute_b32 v38, v17, v18
	s_waitcnt lgkmcnt(1)
	v_add_f32_e32 v23, v23, v25
	s_waitcnt lgkmcnt(0)
	v_add_f32_e32 v25, v18, v38
	v_xor_b32_e32 v18, 4, v19
	v_cmp_lt_i32_e32 vcc, v18, v27
	s_nop 1
	v_cndmask_b32_e32 v18, v19, v18, vcc
	v_lshlrev_b32_e32 v18, 2, v18
	ds_bpermute_b32 v38, v18, v23
	ds_bpermute_b32 v39, v18, v25
	s_waitcnt lgkmcnt(1)
	v_add_f32_e32 v23, v23, v38
	v_xor_b32_e32 v38, 8, v19
	v_cmp_lt_i32_e32 vcc, v38, v27
	s_waitcnt lgkmcnt(0)
	v_add_f32_e32 v25, v25, v39
	v_cndmask_b32_e32 v19, v19, v38, vcc
	v_lshlrev_b32_e32 v19, 2, v19
	ds_bpermute_b32 v27, v19, v23
	ds_bpermute_b32 v38, v19, v25
	v_cmp_gt_i32_e32 vcc, s37, v22
	s_and_b64 s[12:13], s[4:5], vcc
	s_and_saveexec_b64 s[0:1], s[12:13]
	s_cbranch_execz .LBB4_75
	s_waitcnt lgkmcnt(1)
	v_add_f32_e32 v40, v23, v27
	s_ashr_i32 s41, s40, 31
	v_mov_b32_e32 v27, 0
	v_lshl_add_u64 v[22:23], s[40:41], 0, v[26:27]
	v_lshlrev_b64 v[22:23], 2, v[22:23]
	s_waitcnt lgkmcnt(0)
	v_add_f32_e32 v25, v25, v38
	v_lshl_add_u64 v[38:39], s[10:11], 0, v[22:23]
	v_lshl_add_u64 v[22:23], s[8:9], 0, v[22:23]
	global_store_dword v[22:23], v40, off offset:128 sc1
	global_store_dword v[38:39], v25, off offset:128 sc1
.LBB4_75:
	s_or_b64 exec, exec, s[0:1]
	s_waitcnt lgkmcnt(0)
	ds_read_b128 v[38:41], v31
	s_waitcnt lgkmcnt(0)
	v_fma_mix_f32 v4, v4, v38, 0 op_sel_hi:[0,1,0]
	v_fma_mix_f32 v12, v12, v38, 0 op_sel_hi:[0,1,0]
	v_fma_mix_f32 v4, v5, v38, v4 op_sel:[0,1,0] op_sel_hi:[0,1,0]
	v_fma_mix_f32 v5, v13, v38, v12 op_sel:[0,1,0] op_sel_hi:[0,1,0]
	v_fma_mix_f32 v4, v6, v39, v4 op_sel_hi:[0,1,0]
	v_fma_mix_f32 v5, v14, v39, v5 op_sel_hi:[0,1,0]
	v_fma_mix_f32 v4, v7, v39, v4 op_sel:[0,1,0] op_sel_hi:[0,1,0]
	v_fma_mix_f32 v5, v15, v39, v5 op_sel:[0,1,0] op_sel_hi:[0,1,0]
	v_fma_mix_f32 v0, v0, v40, v4 op_sel_hi:[0,1,0]
	v_fma_mix_f32 v4, v8, v40, v5 op_sel_hi:[0,1,0]
	v_fma_mix_f32 v0, v1, v40, v0 op_sel:[0,1,0] op_sel_hi:[0,1,0]
	v_fma_mix_f32 v1, v9, v40, v4 op_sel:[0,1,0] op_sel_hi:[0,1,0]
	v_fma_mix_f32 v0, v2, v41, v0 op_sel_hi:[0,1,0]
	v_fma_mix_f32 v1, v10, v41, v1 op_sel_hi:[0,1,0]
	v_fma_mix_f32 v0, v3, v41, v0 op_sel:[0,1,0] op_sel_hi:[0,1,0]
	v_fma_mix_f32 v1, v11, v41, v1 op_sel:[0,1,0] op_sel_hi:[0,1,0]
	ds_bpermute_b32 v2, v16, v0
	ds_bpermute_b32 v3, v16, v1
	v_or_b32_e32 v6, s40, v28
	v_mad_i64_i32 v[4:5], s[0:1], v6, s36, 0
	s_waitcnt lgkmcnt(1)
	v_add_f32_e32 v0, v0, v2
	s_waitcnt lgkmcnt(0)
	v_add_f32_e32 v1, v1, v3
	ds_bpermute_b32 v2, v17, v0
	ds_bpermute_b32 v3, v17, v1
	v_cmp_gt_i32_e32 vcc, s37, v6
	v_lshl_add_u64 v[4:5], v[4:5], 1, v[20:21]
	s_and_b64 s[4:5], s[4:5], vcc
	s_waitcnt lgkmcnt(1)
	v_add_f32_e32 v0, v0, v2
	s_waitcnt lgkmcnt(0)
	v_add_f32_e32 v1, v1, v3
	ds_bpermute_b32 v2, v18, v0
	ds_bpermute_b32 v3, v18, v1
	global_store_dwordx4 v[4:5], v[38:41], off sc1
	s_waitcnt lgkmcnt(1)
	v_add_f32_e32 v0, v0, v2
	s_waitcnt lgkmcnt(0)
	v_add_f32_e32 v1, v1, v3
	ds_bpermute_b32 v2, v19, v0
	ds_bpermute_b32 v3, v19, v1
	s_and_saveexec_b64 s[0:1], s[4:5]
	s_cbranch_execz .LBB4_77
	s_ashr_i32 s41, s40, 31
	v_mov_b32_e32 v27, 0
	s_waitcnt lgkmcnt(0)
	v_add_f32_e32 v4, v1, v3
	v_add_f32_e32 v5, v0, v2
	v_lshl_add_u64 v[0:1], s[40:41], 0, v[26:27]
	v_lshlrev_b64 v[0:1], 2, v[0:1]
	v_lshl_add_u64 v[2:3], s[10:11], 0, v[0:1]
	v_lshl_add_u64 v[0:1], s[8:9], 0, v[0:1]
	global_store_dword v[0:1], v5, off offset:192 sc1
	global_store_dword v[2:3], v4, off offset:192 sc1

.LBB4_79:
	s_and_b64 vcc, exec, s[0:1]
	s_cbranch_vccz .LBB4_81
	s_waitcnt vmcnt(5) lgkmcnt(0)
	ds_read_b128 v[0:3], v31
	s_waitcnt vmcnt(4)
	v_or_b32_e32 v4, s40, v28
	v_mad_i64_i32 v[4:5], s[0:1], v4, s36, 0
	v_lshl_add_u64 v[4:5], v[4:5], 1, v[20:21]
	s_waitcnt lgkmcnt(0)
	global_store_dwordx4 v[4:5], v[0:3], off sc1

.LBB4_87:
	s_or_b64 exec, exec, s[6:7]
	s_waitcnt lgkmcnt(0)
	s_barrier
	s_and_saveexec_b64 s[6:7], s[2:3]
	s_cbranch_execz .LBB4_89
	s_ashr_i32 s8, s30, 31
	s_mul_i32 s9, s30, s11
	s_mul_hi_u32 s11, s30, s5
	s_add_i32 s9, s11, s9
	s_mul_i32 s8, s8, s5
	s_add_i32 s9, s9, s8
	s_mul_i32 s8, s30, s5
	s_lshl_b64 s[8:9], s[8:9], 7
	s_add_u32 s8, s22, s8
	s_addc_u32 s9, s23, s9
	s_ashr_i32 s5, s4, 31
	s_lshl_b64 s[4:5], s[4:5], 1
	s_add_u32 s4, s8, s4
	s_addc_u32 s5, s9, s5
	v_lshlrev_b32_e32 v0, 1, v24
	v_mov_b32_e32 v1, 0
	s_waitcnt vmcnt(3)
	v_lshl_add_u64 v[8:9], s[4:5], 0, v[0:1]
	ds_read_b128 v[0:3], v34
	v_or_b32_e32 v4, s10, v26
	v_mad_i64_i32 v[4:5], s[4:5], v4, s28, 0
	v_lshl_add_u64 v[10:11], v[4:5], 1, v[8:9]
	ds_read_b128 v[4:7], v33
	s_waitcnt lgkmcnt(1)
	global_store_dwordx4 v[10:11], v[0:3], off sc1
	s_nop 1
	v_or_b32_e32 v0, s10, v30
	v_mad_i64_i32 v[0:1], s[4:5], v0, s28, 0
	v_lshl_add_u64 v[0:1], v[0:1], 1, v[8:9]
	s_waitcnt lgkmcnt(0)
	global_store_dwordx4 v[0:1], v[4:7], off sc1
	ds_read_b128 v[0:3], v32
	s_nop 0
	v_or_b32_e32 v4, s10, v29
	v_mad_i64_i32 v[4:5], s[4:5], v4, s28, 0
	v_lshl_add_u64 v[10:11], v[4:5], 1, v[8:9]
	ds_read_b128 v[4:7], v31
	s_waitcnt lgkmcnt(1)
	global_store_dwordx4 v[10:11], v[0:3], off sc1
	s_nop 1
	v_or_b32_e32 v0, s10, v28
	v_mad_i64_i32 v[0:1], s[4:5], v0, s28, 0
	v_lshl_add_u64 v[0:1], v[0:1], 1, v[8:9]
	s_waitcnt lgkmcnt(0)
	global_store_dwordx4 v[0:1], v[4:7], off sc1

.LBB4_97:
	s_or_b64 exec, exec, s[4:5]
	s_waitcnt lgkmcnt(0)
	s_barrier
	s_and_saveexec_b64 s[4:5], s[2:3]
	s_cbranch_execz .LBB4_40
	s_ashr_i32 s2, s26, 31
	s_mul_i32 s3, s26, s9
	s_mul_hi_u32 s4, s26, s1
	s_add_i32 s3, s4, s3
	s_mul_i32 s2, s2, s1
	s_add_i32 s3, s3, s2
	s_mul_i32 s2, s26, s1
	s_lshl_b64 s[2:3], s[2:3], 7
	s_add_u32 s2, s18, s2
	s_addc_u32 s3, s19, s3
	s_ashr_i32 s1, s0, 31
	s_lshl_b64 s[0:1], s[0:1], 1
	s_add_u32 s0, s2, s0
	s_addc_u32 s1, s3, s1
	v_lshlrev_b32_e32 v0, 1, v24
	v_mov_b32_e32 v1, 0
	s_waitcnt vmcnt(3)
	v_lshl_add_u64 v[8:9], s[0:1], 0, v[0:1]
	ds_read_b128 v[0:3], v34
	v_or_b32_e32 v4, s8, v26
	v_mad_i64_i32 v[4:5], s[0:1], v4, s24, 0
	v_lshl_add_u64 v[10:11], v[4:5], 1, v[8:9]
	ds_read_b128 v[4:7], v33
	s_waitcnt lgkmcnt(1)
	global_store_dwordx4 v[10:11], v[0:3], off sc1
	s_nop 1
	v_or_b32_e32 v0, s8, v30
	v_mad_i64_i32 v[0:1], s[0:1], v0, s24, 0
	v_lshl_add_u64 v[0:1], v[0:1], 1, v[8:9]
	s_waitcnt lgkmcnt(0)
	global_store_dwordx4 v[0:1], v[4:7], off sc1
	ds_read_b128 v[0:3], v32
	s_nop 0
	v_or_b32_e32 v4, s8, v29
	v_mad_i64_i32 v[4:5], s[0:1], v4, s24, 0
	v_lshl_add_u64 v[10:11], v[4:5], 1, v[8:9]
	ds_read_b128 v[4:7], v31
	s_waitcnt lgkmcnt(1)
	global_store_dwordx4 v[10:11], v[0:3], off sc1
	s_nop 1
	v_or_b32_e32 v0, s8, v28
	v_mad_i64_i32 v[0:1], s[0:1], v0, s24, 0
	v_lshl_add_u64 v[0:1], v[0:1], 1, v[8:9]
	s_waitcnt lgkmcnt(0)
	global_store_dwordx4 v[0:1], v[4:7], off sc1
	s_endpgm
	.p2align	8

.LBB5_24:
	s_lshr_b32 s2, s7, 30
	s_add_i32 s2, s7, s2
	s_and_b32 s2, s2, 0x1ffffc
	s_sub_i32 s2, s7, s2
	s_mul_i32 s2, s2, 0x8800
	s_add_i32 s2, s2, 0
	v_lshlrev_b32_e32 v40, 2, v45
	v_add_u32_e32 v42, s2, v44
	v_add_u32_e32 v45, s2, v43
	v_add_u32_e32 v50, v42, v41
	v_add_u32_e32 v62, v45, v41
	s_waitcnt vmcnt(2)
	s_barrier
	ds_read_b128 v[46:49], v50
	ds_read_b128 v[50:53], v50 offset:2048
	ds_read_b128 v[54:57], v62 offset:16384
	ds_read_b128 v[58:61], v62 offset:18432
	ds_read_b128 v[62:65], v62 offset:20480
	v_add_u32_e32 v42, v42, v39
	s_add_i32 s2, s22, -1
	s_waitcnt lgkmcnt(0)
	v_mfma_f32_16x16x32_f16 v[18:21], v[54:57], v[46:49], v[18:21]
	s_lshr_b32 s3, s2, 30
	s_add_i32 s3, s2, s3
	s_and_b32 s3, s3, 0x1ffffc
	v_mfma_f32_16x16x32_f16 v[34:37], v[58:61], v[46:49], v[34:37]
	s_sub_i32 s2, s2, s3
	s_mul_i32 s2, s2, 0x8800
	s_add_i32 s2, s2, 0
	v_mfma_f32_16x16x32_f16 v[26:29], v[62:65], v[46:49], v[26:29]
	v_lshl_add_u32 v38, v38, 5, s11
	v_mfma_f32_16x16x32_f16 v[30:33], v[54:57], v[50:53], v[30:33]
	v_mfma_f32_16x16x32_f16 v[22:25], v[58:61], v[50:53], v[22:25]
	v_mfma_f32_16x16x32_f16 v[14:17], v[62:65], v[50:53], v[14:17]
	ds_read_b128 v[46:49], v42
	ds_read_b128 v[50:53], v42 offset:2048
	v_add_u32_e32 v42, v45, v39
	ds_read_b128 v[54:57], v42 offset:16384
	ds_read_b128 v[58:61], v42 offset:18432
	ds_read_b128 v[62:65], v42 offset:20480
	s_waitcnt lgkmcnt(0)
	v_mfma_f32_16x16x32_f16 v[26:29], v[62:65], v[46:49], v[26:29]
	s_waitcnt vmcnt(0)
	s_barrier
	v_mfma_f32_16x16x32_f16 v[14:17], v[62:65], v[50:53], v[14:17]
	v_add_u32_e32 v62, s2, v44
	v_add_u32_e32 v63, s2, v43
	v_mfma_f32_16x16x32_f16 v[18:21], v[54:57], v[46:49], v[18:21]
	v_mfma_f32_16x16x32_f16 v[34:37], v[58:61], v[46:49], v[34:37]
	v_add_u32_e32 v46, v62, v41
	v_add_u32_e32 v41, v63, v41
	ds_read_b128 v[42:45], v46
	ds_read_b128 v[46:49], v46 offset:2048
	v_mfma_f32_16x16x32_f16 v[30:33], v[54:57], v[50:53], v[30:33]
	v_mfma_f32_16x16x32_f16 v[22:25], v[58:61], v[50:53], v[22:25]
	ds_read_b128 v[50:53], v41 offset:16384
	ds_read_b128 v[54:57], v41 offset:18432
	ds_read_b128 v[58:61], v41 offset:20480
	v_add_u32_e32 v41, v62, v39
	v_add_u32_e32 v39, v63, v39
	s_waitcnt lgkmcnt(2)
	v_mfma_f32_16x16x32_f16 v[18:21], v[50:53], v[42:45], v[18:21]
	s_waitcnt lgkmcnt(1)
	v_mfma_f32_16x16x32_f16 v[34:37], v[54:57], v[42:45], v[34:37]
	s_waitcnt lgkmcnt(0)
	v_mfma_f32_16x16x32_f16 v[26:29], v[58:61], v[42:45], v[26:29]
	v_mfma_f32_16x16x32_f16 v[30:33], v[50:53], v[46:49], v[30:33]
	v_mfma_f32_16x16x32_f16 v[22:25], v[54:57], v[46:49], v[22:25]
	v_mfma_f32_16x16x32_f16 v[14:17], v[58:61], v[46:49], v[14:17]
	ds_read_b128 v[42:45], v41
	ds_read_b128 v[46:49], v41 offset:2048
	ds_read_b128 v[50:53], v39 offset:16384
	ds_read_b128 v[54:57], v39 offset:18432
	ds_read_b128 v[58:61], v39 offset:20480
	v_or_b32_e32 v41, v38, v0
	s_waitcnt lgkmcnt(2)
	v_mfma_f32_16x16x32_f16 v[18:21], v[50:53], v[42:45], v[18:21]
	v_or_b32_e32 v0, v1, v40
	v_add_u32_e32 v0, s6, v0
	v_mad_i64_i32 v[38:39], s[2:3], v41, s9, 0
	s_waitcnt lgkmcnt(1)
	v_mfma_f32_16x16x32_f16 v[34:37], v[54:57], v[42:45], v[34:37]
	v_ashrrev_i32_e32 v1, 31, v0
	v_lshl_add_u64 v[38:39], v[38:39], 1, s[0:1]
	s_waitcnt vmcnt(2)
	v_pk_add_f32 v[18:19], v[10:11], v[18:19]
	s_waitcnt lgkmcnt(0)
	v_mfma_f32_16x16x32_f16 v[26:29], v[58:61], v[42:45], v[26:29]
	v_add_f32_e64 v20, v12, v20
	v_add_f32_e64 v21, v13, v21
	v_lshlrev_b64 v[0:1], 1, v[0:1]
	v_cvt_pk_f16_f32 v18, v18, v19
	v_cvt_pk_f16_f32 v19, v20, v21
	v_lshl_add_u64 v[20:21], v[38:39], 0, v[0:1]
	v_mfma_f32_16x16x32_f16 v[30:33], v[50:53], v[46:49], v[30:33]
	global_store_dwordx2 v[20:21], v[18:19], off sc1
	s_waitcnt vmcnt(2)
	v_pk_add_f32 v[18:19], v[6:7], v[34:35]
	v_pk_add_f32 v[34:35], v[8:9], v[36:37]
	v_cvt_pk_f16_f32 v18, v18, v19
	v_cvt_pk_f16_f32 v19, v34, v35
	global_store_dwordx2 v[20:21], v[18:19], off offset:32 sc1
	s_waitcnt vmcnt(2)
	v_pk_add_f32 v[18:19], v[2:3], v[26:27]
	v_pk_add_f32 v[26:27], v[4:5], v[28:29]
	v_cvt_pk_f16_f32 v18, v18, v19
	v_cvt_pk_f16_f32 v19, v26, v27
	global_store_dwordx2 v[20:21], v[18:19], off offset:64 sc1
	v_add_f32_e32 v20, v10, v30
	v_add_f32_e32 v21, v13, v33
	v_pk_mov_b32 v[10:11], v[10:11], v[12:13] op_sel:[1,0]
	v_mov_b32_e32 v12, v31
	v_mov_b32_e32 v13, v32
	v_cvt_f16_f32_e32 v20, v20
	v_pk_add_f32 v[10:11], v[10:11], v[12:13]
	v_cvt_f16_f32_e32 v12, v21
	v_mfma_f32_16x16x32_f16 v[22:25], v[54:57], v[46:49], v[22:25]
	v_or_b32_e32 v18, 16, v41
	v_mad_i64_i32 v[18:19], s[2:3], v18, s9, 0
	v_lshl_add_u64 v[18:19], v[18:19], 1, s[0:1]
	v_cvt_pk_f16_f32 v11, v10, v11
	v_pack_b32_f16 v10, v20, v11
	v_alignbit_b32 v11, v12, v11, 16
	v_lshl_add_u64 v[0:1], v[18:19], 0, v[0:1]
	global_store_dwordx2 v[0:1], v[10:11], off sc1
	v_add_f32_e32 v10, v6, v22
	v_add_f32_e32 v11, v9, v25
	v_pk_mov_b32 v[6:7], v[6:7], v[8:9] op_sel:[1,0]
	v_mov_b32_e32 v8, v23
	v_mov_b32_e32 v9, v24
	v_cvt_f16_f32_e32 v10, v10
	v_pk_add_f32 v[6:7], v[6:7], v[8:9]
	v_cvt_f16_f32_e32 v8, v11
	v_mfma_f32_16x16x32_f16 v[14:17], v[58:61], v[46:49], v[14:17]
	v_cvt_pk_f16_f32 v7, v6, v7
	v_pack_b32_f16 v6, v10, v7
	v_alignbit_b32 v7, v8, v7, 16
	global_store_dwordx2 v[0:1], v[6:7], off offset:32 sc1
	s_nop 3
	v_add_f32_e32 v6, v2, v14
	v_add_f32_e32 v7, v5, v17
	v_pk_mov_b32 v[2:3], v[2:3], v[4:5] op_sel:[1,0]
	v_mov_b32_e32 v4, v15
	v_mov_b32_e32 v5, v16
	v_cvt_f16_f32_e32 v6, v6
	v_pk_add_f32 v[2:3], v[2:3], v[4:5]
	v_cvt_f16_f32_e32 v4, v7
	v_cvt_pk_f16_f32 v3, v2, v3
	v_pack_b32_f16 v2, v6, v3
	v_alignbit_b32 v3, v4, v3, 16
	global_store_dwordx2 v[0:1], v[2:3], off offset:64 sc1
	s_endpgm
	.p2align	8

.LBB6_41:
	s_or_b64 exec, exec, s[0:1]
	v_lshlrev_b32_e32 v0, 3, v55
	v_lshl_or_b32 v0, v56, 8, v0
	v_add_u32_e32 v0, 0x1800, v0
	s_waitcnt lgkmcnt(0)
	s_barrier
	ds_read2_b64 v[38:41], v0 offset0:32 offset1:48
	v_or_b32_e32 v0, v1, v54
	v_lshl_add_u32 v1, v56, 5, s28
	v_or_b32_e32 v81, v1, v55
	v_lshlrev_b32_e32 v80, 2, v0
	v_mad_i64_i32 v[42:43], s[0:1], v81, s13, 0
	v_lshl_add_u64 v[74:75], v[42:43], 1, s[24:25]
	ds_read_b128 v[42:45], v80 offset:4096
	ds_read_b128 v[46:49], v80 offset:4672
	ds_read_b128 v[50:53], v80 offset:5248
	ds_read_b128 v[54:57], v80 offset:5824
	ds_read_b128 v[58:61], v80 offset:4160
	ds_read_b128 v[62:65], v80 offset:4224
	s_waitcnt lgkmcnt(4)
	v_pk_add_f32 v[76:77], v[42:43], v[46:47]
	v_pk_add_f32 v[78:79], v[44:45], v[48:49]
	s_waitcnt lgkmcnt(2)
	v_pk_add_f32 v[54:55], v[50:51], v[54:55]
	v_pk_fma_f32 v[34:35], v[38:39], v[76:77], v[34:35] op_sel_hi:[0,1,1] neg_lo:[1,0,0] neg_hi:[1,0,0]
	v_pk_fma_f32 v[34:35], v[38:39], v[34:35], v[54:55] op_sel:[1,0,0]
	v_pk_add_f32 v[56:57], v[52:53], v[56:57]
	v_pk_add_f32 v[34:35], v[10:11], v[34:35]
	ds_read_b128 v[66:69], v80 offset:5312
	ds_read_b128 v[70:73], v80 offset:5376
	v_cvt_pk_f16_f32 v88, v34, v35
	v_pk_fma_f32 v[34:35], v[38:39], v[78:79], v[36:37] op_sel_hi:[0,1,1] neg_lo:[1,0,0] neg_hi:[1,0,0]
	v_pk_fma_f32 v[34:35], v[38:39], v[34:35], v[56:57] op_sel:[1,0,0]
	v_add_u32_e32 v0, s10, v0
	v_pk_add_f32 v[34:35], v[12:13], v[34:35]
	ds_read_b128 v[42:45], v80 offset:5888
	ds_read_b128 v[50:53], v80 offset:5952
	v_cvt_pk_f16_f32 v89, v34, v35
	ds_read_b128 v[34:37], v80 offset:4736
	v_ashrrev_i32_e32 v1, 31, v0
	v_lshlrev_b64 v[0:1], 1, v[0:1]
	v_lshl_add_u64 v[74:75], v[74:75], 0, v[0:1]
	v_mbcnt_lo_u32_b32 v94, -1, 0
	v_mbcnt_hi_u32_b32 v94, -1, v94
	v_and_b32_e32 v94, 16, v94
	v_lshrrev_b32_e32 v95, 1, v94
	v_add_u32_e32 v94, v94, v95
	v_mov_b32_e32 v95, 0
	ds_read_b128 v[46:49], v80 offset:4800
	s_waitcnt lgkmcnt(1)
	v_pk_add_f32 v[34:35], v[58:59], v[34:35]
	v_pk_add_f32 v[36:37], v[60:61], v[36:37]
	v_pk_add_f32 v[42:43], v[66:67], v[42:43]
	v_pk_fma_f32 v[30:31], v[38:39], v[34:35], v[30:31] op_sel_hi:[0,1,1] neg_lo:[1,0,0] neg_hi:[1,0,0]
	v_pk_add_f32 v[44:45], v[68:69], v[44:45]
	v_pk_fma_f32 v[32:33], v[38:39], v[36:37], v[32:33] op_sel_hi:[0,1,1] neg_lo:[1,0,0] neg_hi:[1,0,0]
	v_pk_fma_f32 v[30:31], v[38:39], v[30:31], v[42:43] op_sel:[1,0,0]
	v_pk_fma_f32 v[32:33], v[38:39], v[32:33], v[44:45] op_sel:[1,0,0]
	v_pk_add_f32 v[30:31], v[6:7], v[30:31]
	v_pk_add_f32 v[32:33], v[8:9], v[32:33]
	v_cvt_pk_f16_f32 v90, v30, v31
	v_cvt_pk_f16_f32 v91, v32, v33
	v_lshl_add_u64 v[92:93], v[74:75], 0, v[94:95]
	s_nop 1
	v_permlane16_swap_b32 v88, v90
	v_permlane16_swap_b32 v89, v91
	global_store_dwordx4 v[92:93], v[88:91], off sc1
	s_waitcnt lgkmcnt(0)
	v_pk_add_f32 v[30:31], v[62:63], v[46:47]
	v_pk_add_f32 v[46:47], v[64:65], v[48:49]
	v_pk_add_f32 v[32:33], v[70:71], v[50:51]
	v_pk_fma_f32 v[26:27], v[38:39], v[30:31], v[26:27] op_sel_hi:[0,1,1] neg_lo:[1,0,0] neg_hi:[1,0,0]
	v_pk_add_f32 v[48:49], v[72:73], v[52:53]
	v_pk_fma_f32 v[28:29], v[38:39], v[46:47], v[28:29] op_sel_hi:[0,1,1] neg_lo:[1,0,0] neg_hi:[1,0,0]
	v_pk_fma_f32 v[26:27], v[38:39], v[26:27], v[32:33] op_sel:[1,0,0]
	v_pk_fma_f32 v[28:29], v[38:39], v[28:29], v[48:49] op_sel:[1,0,0]
	v_pk_add_f32 v[26:27], v[2:3], v[26:27]
	v_pk_add_f32 v[28:29], v[4:5], v[28:29]
	v_pk_fma_f32 v[22:23], v[40:41], v[76:77], v[22:23] op_sel_hi:[0,1,1] neg_lo:[1,0,0] neg_hi:[1,0,0]
	v_cvt_pk_f16_f32 v100, v26, v27
	v_cvt_pk_f16_f32 v101, v28, v29
	v_pk_fma_f32 v[22:23], v[40:41], v[22:23], v[54:55] op_sel:[1,0,0]
	v_or_b32_e32 v26, 16, v81
	v_pk_add_f32 v[10:11], v[10:11], v[22:23]
	v_pk_fma_f32 v[22:23], v[40:41], v[78:79], v[24:25] op_sel_hi:[0,1,1] neg_lo:[1,0,0] neg_hi:[1,0,0]
	v_mad_i64_i32 v[26:27], s[0:1], v26, s13, 0
	v_pk_fma_f32 v[22:23], v[40:41], v[22:23], v[56:57] op_sel:[1,0,0]
	v_lshl_add_u64 v[26:27], v[26:27], 1, s[24:25]
	v_pk_add_f32 v[12:13], v[12:13], v[22:23]
	v_cvt_pk_f16_f32 v96, v10, v11
	v_cvt_pk_f16_f32 v97, v12, v13
	v_lshl_add_u64 v[0:1], v[26:27], 0, v[0:1]
	v_pk_fma_f32 v[10:11], v[40:41], v[34:35], v[18:19] op_sel_hi:[0,1,1] neg_lo:[1,0,0] neg_hi:[1,0,0]
	v_pk_fma_f32 v[10:11], v[40:41], v[10:11], v[42:43] op_sel:[1,0,0]
	s_nop 0
	v_pk_add_f32 v[6:7], v[6:7], v[10:11]
	v_pk_fma_f32 v[10:11], v[40:41], v[36:37], v[20:21] op_sel_hi:[0,1,1] neg_lo:[1,0,0] neg_hi:[1,0,0]
	v_pk_fma_f32 v[10:11], v[40:41], v[10:11], v[44:45] op_sel:[1,0,0]
	v_cvt_pk_f16_f32 v98, v6, v7
	v_pk_add_f32 v[8:9], v[8:9], v[10:11]
	s_nop 0
	v_cvt_pk_f16_f32 v99, v8, v9
	v_lshl_add_u64 v[92:93], v[0:1], 0, v[94:95]
	s_nop 1
	v_permlane16_swap_b32 v96, v98
	v_permlane16_swap_b32 v97, v99
	global_store_dwordx4 v[92:93], v[96:99], off sc1
	v_pk_fma_f32 v[6:7], v[40:41], v[30:31], v[14:15] op_sel_hi:[0,1,1] neg_lo:[1,0,0] neg_hi:[1,0,0]
	v_pk_fma_f32 v[6:7], v[40:41], v[6:7], v[32:33] op_sel:[1,0,0]
	s_nop 0
	v_pk_add_f32 v[2:3], v[2:3], v[6:7]
	v_pk_fma_f32 v[6:7], v[40:41], v[46:47], v[16:17] op_sel_hi:[0,1,1] neg_lo:[1,0,0] neg_hi:[1,0,0]
	v_pk_fma_f32 v[6:7], v[40:41], v[6:7], v[48:49] op_sel:[1,0,0]
	v_cvt_pk_f16_f32 v102, v2, v3
	v_pk_add_f32 v[4:5], v[4:5], v[6:7]
	s_nop 0
	v_cvt_pk_f16_f32 v103, v4, v5
	v_bfe_u32 v95, v94, 3, 1
	v_mul_u32_u24_e32 v94, 0x11ff8, v95
	v_add_u32_e32 v94, 0xfffee040, v94
	v_add_u32_e32 v95, -1, v95
	v_lshl_add_u64 v[92:93], v[0:1], 0, v[94:95]
	v_permlane16_swap_b32 v100, v102
	v_permlane16_swap_b32 v101, v103
	global_store_dwordx4 v[92:93], v[100:103], off sc1
	s_endpgm
	.p2align	8

.LBB7_9:
	s_lshr_b32 s4, s3, 29
	s_add_i32 s4, s3, s4
	s_and_b32 s4, s4, 0xffff8
	s_sub_i32 s3, s3, s4
	s_mulk_i32 s3, 0x5000
	s_add_i32 s3, s3, 0
	v_add_u32_e32 v68, s3, v43
	v_lshlrev_b32_e32 v69, 1, v46
	v_add_u32_e32 v45, s3, v0
	v_add_u32_e32 v44, v68, v69
	v_add_u32_e32 v46, v45, v69
	s_waitcnt vmcnt(25)
	s_barrier
	ds_read_b128 v[48:51], v44 offset:8192
	ds_read_b128 v[52:55], v46
	ds_read_b128 v[56:59], v44 offset:10240
	ds_read_b128 v[60:63], v46 offset:2048
	ds_read_b128 v[64:67], v44 offset:12288
	v_lshlrev_b32_e32 v70, 1, v47
	s_waitcnt lgkmcnt(2)
	v_mfma_f32_16x16x32_f16 a[4:7], v[56:59], v[52:55], a[4:7]
	v_add_u32_e32 v71, v45, v70
	s_add_i32 s3, s15, -5
	s_lshr_b32 s4, s3, 29
	s_waitcnt lgkmcnt(1)
	v_mfma_f32_16x16x32_f16 a[16:19], v[56:59], v[60:63], a[16:19]
	v_add_u32_e32 v56, v68, v70
	s_add_i32 s4, s3, s4
	s_and_b32 s4, s4, 0xffff8
	v_mfma_f32_16x16x32_f16 a[0:3], v[48:51], v[52:55], a[0:3]
	s_sub_i32 s3, s3, s4
	s_mulk_i32 s3, 0x5000
	s_add_i32 s3, s3, 0
	v_mfma_f32_16x16x32_f16 a[12:15], v[48:51], v[60:63], a[12:15]
	ds_read_b128 v[48:51], v56 offset:8192
	ds_read_b128 v[44:47], v71
	v_add_u32_e32 v68, s3, v43
	s_waitcnt lgkmcnt(2)
	v_mfma_f32_16x16x32_f16 a[8:11], v[64:67], v[52:55], a[8:11]
	ds_read_b128 v[52:55], v56 offset:10240
	ds_read_b128 v[56:59], v56 offset:12288
	v_lshlrev_b32_e32 v42, 2, v42
	s_waitcnt lgkmcnt(2)
	v_mfma_f32_16x16x32_f16 a[0:3], v[48:51], v[44:47], a[0:3]
	v_lshl_add_u64 v[40:41], v[40:41], 2, s[0:1]
	s_waitcnt lgkmcnt(1)
	v_mfma_f32_16x16x32_f16 a[4:7], v[52:55], v[44:47], a[4:7]
	s_waitcnt lgkmcnt(0)
	v_mfma_f32_16x16x32_f16 a[8:11], v[56:59], v[44:47], a[8:11]
	ds_read_b128 v[44:47], v71 offset:2048
	s_waitcnt vmcnt(20)
	s_barrier
	v_mfma_f32_16x16x32_f16 a[20:23], v[64:67], v[60:63], a[20:23]
	v_add_u32_e32 v64, s3, v0
	v_add_u32_e32 v60, v68, v69
	s_add_i32 s3, s15, -4
	s_waitcnt lgkmcnt(0)
	v_mfma_f32_16x16x32_f16 a[20:23], v[56:59], v[44:47], a[20:23]
	v_add_u32_e32 v56, v64, v69
	v_add_u32_e32 v71, v64, v70
	s_lshr_b32 s4, s3, 29
	v_mfma_f32_16x16x32_f16 a[12:15], v[48:51], v[44:47], a[12:15]
	s_add_i32 s4, s3, s4
	s_and_b32 s4, s4, 0xffff8
	s_sub_i32 s3, s3, s4
	v_mfma_f32_16x16x32_f16 a[16:19], v[52:55], v[44:47], a[16:19]
	ds_read_b128 v[44:47], v60 offset:8192
	ds_read_b128 v[48:51], v60 offset:10240
	ds_read_b128 v[52:55], v56
	ds_read_b128 v[56:59], v56 offset:2048
	ds_read_b128 v[60:63], v60 offset:12288
	s_waitcnt lgkmcnt(2)
	v_mfma_f32_16x16x32_f16 a[0:3], v[44:47], v[52:55], a[0:3]
	ds_read_b128 v[64:67], v71
	s_mulk_i32 s3, 0x5000
	s_add_i32 s3, s3, 0
	v_mfma_f32_16x16x32_f16 a[4:7], v[48:51], v[52:55], a[4:7]
	s_waitcnt lgkmcnt(1)
	v_mfma_f32_16x16x32_f16 a[8:11], v[60:63], v[52:55], a[8:11]
	v_add_u32_e32 v52, v68, v70
	v_add_u32_e32 v68, s3, v43
	v_mfma_f32_16x16x32_f16 a[12:15], v[44:47], v[56:59], a[12:15]
	ds_read_b128 v[44:47], v52 offset:8192
	v_mfma_f32_16x16x32_f16 a[16:19], v[48:51], v[56:59], a[16:19]
	ds_read_b128 v[48:51], v52 offset:10240
	ds_read_b128 v[52:55], v52 offset:12288
	v_mfma_f32_16x16x32_f16 a[20:23], v[60:63], v[56:59], a[20:23]
	ds_read_b128 v[56:59], v71 offset:2048
	v_add_u32_e32 v60, v68, v69
	s_waitcnt vmcnt(15)
	s_waitcnt lgkmcnt(3)
	v_mfma_f32_16x16x32_f16 a[0:3], v[44:47], v[64:67], a[0:3]
	s_barrier
	v_add_u32_e32 v68, v68, v70
	s_waitcnt lgkmcnt(0)
	v_mfma_f32_16x16x32_f16 a[12:15], v[44:47], v[56:59], a[12:15]
	ds_read_b128 v[44:47], v60 offset:8192
	v_mfma_f32_16x16x32_f16 a[4:7], v[48:51], v[64:67], a[4:7]
	v_mfma_f32_16x16x32_f16 a[8:11], v[52:55], v[64:67], a[8:11]
	v_add_u32_e32 v64, s3, v0
	s_add_i32 s3, s15, -3
	s_lshr_b32 s4, s3, 29
	v_mfma_f32_16x16x32_f16 a[16:19], v[48:51], v[56:59], a[16:19]
	s_add_i32 s4, s3, s4
	v_add_u32_e32 v71, v64, v70
	s_and_b32 s4, s4, 0xffff8
	v_mfma_f32_16x16x32_f16 a[20:23], v[52:55], v[56:59], a[20:23]
	v_add_u32_e32 v56, v64, v69
	ds_read_b128 v[48:51], v60 offset:10240
	ds_read_b128 v[52:55], v56
	ds_read_b128 v[56:59], v56 offset:2048
	ds_read_b128 v[60:63], v60 offset:12288
	s_waitcnt lgkmcnt(2)
	v_mfma_f32_16x16x32_f16 a[0:3], v[44:47], v[52:55], a[0:3]
	ds_read_b128 v[64:67], v71
	s_sub_i32 s3, s3, s4
	s_mulk_i32 s3, 0x5000
	s_waitcnt lgkmcnt(2)
	v_mfma_f32_16x16x32_f16 a[12:15], v[44:47], v[56:59], a[12:15]
	ds_read_b128 v[44:47], v68 offset:8192
	s_add_i32 s3, s3, 0
	v_mfma_f32_16x16x32_f16 a[4:7], v[48:51], v[52:55], a[4:7]
	s_waitcnt lgkmcnt(2)
	v_mfma_f32_16x16x32_f16 a[8:11], v[60:63], v[52:55], a[8:11]
	v_mfma_f32_16x16x32_f16 a[16:19], v[48:51], v[56:59], a[16:19]
	v_mfma_f32_16x16x32_f16 a[20:23], v[60:63], v[56:59], a[20:23]
	ds_read_b128 v[48:51], v68 offset:10240
	ds_read_b128 v[52:55], v71 offset:2048
	ds_read_b128 v[56:59], v68 offset:12288
	v_add_u32_e32 v68, s3, v43
	v_add_u32_e32 v60, v68, v69
	s_waitcnt lgkmcnt(3)
	v_mfma_f32_16x16x32_f16 a[0:3], v[44:47], v[64:67], a[0:3]
	s_waitcnt vmcnt(10)
	s_barrier
	v_add_u32_e32 v68, v68, v70
	s_waitcnt lgkmcnt(1)
	v_mfma_f32_16x16x32_f16 a[12:15], v[44:47], v[52:55], a[12:15]
	ds_read_b128 v[44:47], v60 offset:8192
	v_mfma_f32_16x16x32_f16 a[4:7], v[48:51], v[64:67], a[4:7]
	s_waitcnt lgkmcnt(1)
	v_mfma_f32_16x16x32_f16 a[8:11], v[56:59], v[64:67], a[8:11]
	v_add_u32_e32 v64, s3, v0
	v_add_u32_e32 v61, v64, v69
	s_add_i32 s3, s15, -2
	v_mfma_f32_16x16x32_f16 a[16:19], v[48:51], v[52:55], a[16:19]
	ds_read_b128 v[48:51], v60 offset:10240
	s_lshr_b32 s4, s3, 29
	s_add_i32 s4, s3, s4
	v_mfma_f32_16x16x32_f16 a[20:23], v[56:59], v[52:55], a[20:23]
	ds_read_b128 v[52:55], v61
	ds_read_b128 v[56:59], v61 offset:2048
	ds_read_b128 v[60:63], v60 offset:12288
	v_add_u32_e32 v71, v64, v70
	s_waitcnt lgkmcnt(2)
	v_mfma_f32_16x16x32_f16 a[0:3], v[44:47], v[52:55], a[0:3]
	s_and_b32 s4, s4, 0xffff8
	ds_read_b128 v[64:67], v71
	s_sub_i32 s3, s3, s4
	s_waitcnt lgkmcnt(2)
	v_mfma_f32_16x16x32_f16 a[12:15], v[44:47], v[56:59], a[12:15]
	ds_read_b128 v[44:47], v68 offset:8192
	s_mulk_i32 s3, 0x5000
	s_add_i32 s3, s3, 0
	v_mfma_f32_16x16x32_f16 a[4:7], v[48:51], v[52:55], a[4:7]
	s_waitcnt lgkmcnt(2)
	v_mfma_f32_16x16x32_f16 a[8:11], v[60:63], v[52:55], a[8:11]
	v_mfma_f32_16x16x32_f16 a[16:19], v[48:51], v[56:59], a[16:19]
	v_mfma_f32_16x16x32_f16 a[20:23], v[60:63], v[56:59], a[20:23]
	ds_read_b128 v[48:51], v68 offset:10240
	ds_read_b128 v[52:55], v71 offset:2048
	ds_read_b128 v[56:59], v68 offset:12288
	v_add_u32_e32 v68, s3, v43
	v_add_u32_e32 v60, v68, v69
	s_waitcnt lgkmcnt(3)
	v_mfma_f32_16x16x32_f16 a[0:3], v[44:47], v[64:67], a[0:3]
	s_waitcnt vmcnt(5)
	s_barrier
	v_add_u32_e32 v68, v68, v70
	s_waitcnt lgkmcnt(1)
	v_mfma_f32_16x16x32_f16 a[12:15], v[44:47], v[52:55], a[12:15]
	ds_read_b128 v[44:47], v60 offset:8192
	v_mfma_f32_16x16x32_f16 a[4:7], v[48:51], v[64:67], a[4:7]
	s_waitcnt lgkmcnt(1)
	v_mfma_f32_16x16x32_f16 a[8:11], v[56:59], v[64:67], a[8:11]
	v_add_u32_e32 v64, s3, v0
	v_add_u32_e32 v61, v64, v69
	s_add_i32 s3, s15, -1
	v_mfma_f32_16x16x32_f16 a[16:19], v[48:51], v[52:55], a[16:19]
	ds_read_b128 v[48:51], v60 offset:10240
	s_lshr_b32 s4, s3, 29
	s_add_i32 s4, s3, s4
	v_mfma_f32_16x16x32_f16 a[20:23], v[56:59], v[52:55], a[20:23]
	ds_read_b128 v[52:55], v61
	ds_read_b128 v[56:59], v61 offset:2048
	ds_read_b128 v[60:63], v60 offset:12288
	v_add_u32_e32 v71, v64, v70
	s_waitcnt lgkmcnt(2)
	v_mfma_f32_16x16x32_f16 a[0:3], v[44:47], v[52:55], a[0:3]
	s_and_b32 s4, s4, 0xffff8
	ds_read_b128 v[64:67], v71
	s_sub_i32 s3, s3, s4
	s_waitcnt lgkmcnt(2)
	v_mfma_f32_16x16x32_f16 a[12:15], v[44:47], v[56:59], a[12:15]
	ds_read_b128 v[44:47], v68 offset:8192
	s_mulk_i32 s3, 0x5000
	s_add_i32 s3, s3, 0
	v_mfma_f32_16x16x32_f16 a[4:7], v[48:51], v[52:55], a[4:7]
	v_add_u32_e32 v43, s3, v43
	v_add_u32_e32 v0, s3, v0
	s_waitcnt lgkmcnt(2)
	v_mfma_f32_16x16x32_f16 a[8:11], v[60:63], v[52:55], a[8:11]
	v_mfma_f32_16x16x32_f16 a[16:19], v[48:51], v[56:59], a[16:19]
	v_mfma_f32_16x16x32_f16 a[20:23], v[60:63], v[56:59], a[20:23]
	ds_read_b128 v[48:51], v68 offset:10240
	ds_read_b128 v[52:55], v71 offset:2048
	ds_read_b128 v[56:59], v68 offset:12288
	v_add_u32_e32 v60, v43, v69
	s_waitcnt vmcnt(0)
	s_waitcnt lgkmcnt(3)
	v_mfma_f32_16x16x32_f16 a[0:3], v[44:47], v[64:67], a[0:3]
	s_barrier
	v_add_u32_e32 v61, v0, v69
	v_add_u32_e32 v43, v43, v70
	s_waitcnt lgkmcnt(1)
	v_mfma_f32_16x16x32_f16 a[12:15], v[44:47], v[52:55], a[12:15]
	ds_read_b128 v[44:47], v60 offset:8192
	v_add_u32_e32 v0, v0, v70
	v_mfma_f32_16x16x32_f16 a[4:7], v[48:51], v[64:67], a[4:7]
	s_waitcnt lgkmcnt(1)
	v_mfma_f32_16x16x32_f16 a[8:11], v[56:59], v[64:67], a[8:11]
	v_mfma_f32_16x16x32_f16 a[16:19], v[48:51], v[52:55], a[16:19]
	ds_read_b128 v[48:51], v60 offset:10240
	v_mfma_f32_16x16x32_f16 a[20:23], v[56:59], v[52:55], a[20:23]
	ds_read_b128 v[52:55], v61
	ds_read_b128 v[56:59], v61 offset:2048
	ds_read_b128 v[60:63], v60 offset:12288
	ds_read_b128 v[64:67], v0
	s_waitcnt lgkmcnt(3)
	v_mfma_f32_16x16x32_f16 a[0:3], v[44:47], v[52:55], a[0:3]
	s_waitcnt lgkmcnt(2)
	v_mfma_f32_16x16x32_f16 a[12:15], v[44:47], v[56:59], a[12:15]
	ds_read_b128 v[44:47], v43 offset:8192
	v_mfma_f32_16x16x32_f16 a[4:7], v[48:51], v[52:55], a[4:7]
	v_mfma_f32_16x16x32_f16 a[16:19], v[48:51], v[56:59], a[16:19]
	ds_read_b128 v[48:51], v43 offset:10240
	s_waitcnt lgkmcnt(3)
	v_mfma_f32_16x16x32_f16 a[20:23], v[60:63], v[56:59], a[20:23]
	ds_read_b128 v[56:59], v0 offset:2048
	v_or_b32_e32 v0, v42, v1
	v_add_u32_e32 v0, s2, v0
	s_waitcnt lgkmcnt(2)
	v_mfma_f32_16x16x32_f16 a[0:3], v[44:47], v[64:67], a[0:3]
	v_ashrrev_i32_e32 v1, 31, v0
	v_lshlrev_b64 v[0:1], 2, v[0:1]
	v_lshl_add_u64 v[40:41], v[40:41], 0, v[0:1]
	v_mfma_f32_16x16x32_f16 a[8:11], v[60:63], v[52:55], a[8:11]
	ds_read_b128 v[52:55], v43 offset:12288
	s_waitcnt lgkmcnt(2)
	v_mfma_f32_16x16x32_f16 a[4:7], v[48:51], v[64:67], a[4:7]
	s_nop 0
	v_accvgpr_read_b32 v43, a1
	v_accvgpr_read_b32 v42, a0
	v_accvgpr_read_b32 v61, a3
	v_accvgpr_read_b32 v60, a2
	s_waitcnt vmcnt(4)
	v_pk_add_f32 v[42:43], v[22:23], v[42:43]
	s_waitcnt lgkmcnt(0)
	v_mfma_f32_16x16x32_f16 a[8:11], v[52:55], v[64:67], a[8:11]
	v_add_f32_e64 v34, v34, v42
	v_add_f32_e64 v35, v35, v43
	v_pk_add_f32 v[42:43], v[24:25], v[60:61]
	v_accvgpr_read_b32 v63, a7
	v_pk_add_f32 v[36:37], v[36:37], v[42:43]
	global_store_dwordx4 v[40:41], v[34:37], off sc1
	v_accvgpr_read_b32 v62, a6
	v_mfma_f32_16x16x32_f16 a[12:15], v[44:47], v[56:59], a[12:15]
	v_accvgpr_read_b32 v35, a5
	v_accvgpr_read_b32 v34, a4
	s_waitcnt vmcnt(4)
	v_pk_add_f32 v[34:35], v[10:11], v[34:35]
	v_accvgpr_read_b32 v45, a11
	v_pk_add_f32 v[30:31], v[30:31], v[34:35]
	v_pk_add_f32 v[34:35], v[12:13], v[62:63]
	v_accvgpr_read_b32 v44, a10
	v_pk_add_f32 v[32:33], v[32:33], v[34:35]
	global_store_dwordx4 v[40:41], v[30:33], off offset:64 sc1
	v_mfma_f32_16x16x32_f16 a[16:19], v[48:51], v[56:59], a[16:19]
	v_accvgpr_read_b32 v47, a15
	v_accvgpr_read_b32 v31, a9
	v_accvgpr_read_b32 v30, a8
	s_waitcnt vmcnt(4)
	v_pk_add_f32 v[30:31], v[2:3], v[30:31]
	v_accvgpr_read_b32 v46, a14
	v_pk_add_f32 v[26:27], v[26:27], v[30:31]
	v_pk_add_f32 v[30:31], v[4:5], v[44:45]
	s_nop 0
	v_pk_add_f32 v[28:29], v[28:29], v[30:31]
	global_store_dwordx4 v[40:41], v[26:29], off offset:128 sc1
	v_accvgpr_read_b32 v49, a19
	v_accvgpr_read_b32 v48, a18
	v_lshl_add_u64 v[26:27], v[38:39], 2, s[0:1]
	v_lshl_add_u64 v[26:27], v[26:27], 0, v[0:1]
	v_accvgpr_read_b32 v0, a12
	v_accvgpr_read_b32 v1, a13
	v_pk_add_f32 v[0:1], v[22:23], v[0:1]
	v_mfma_f32_16x16x32_f16 a[18:21], v[52:55], v[56:59], a[20:23]
	v_add_f32_e64 v18, v18, v0
	v_add_f32_e64 v19, v19, v1
	v_pk_add_f32 v[0:1], v[24:25], v[46:47]
	s_nop 0
	v_pk_add_f32 v[20:21], v[20:21], v[0:1]
	v_accvgpr_read_b32 v0, a16
	v_accvgpr_read_b32 v1, a17
	v_pk_add_f32 v[0:1], v[10:11], v[0:1]
	global_store_dwordx4 v[26:27], v[18:21], off sc1
	s_waitcnt vmcnt(5)
	v_pk_add_f32 v[10:11], v[14:15], v[0:1]
	v_pk_add_f32 v[0:1], v[12:13], v[48:49]
	v_accvgpr_read_b32 v51, a21
	v_pk_add_f32 v[12:13], v[16:17], v[0:1]
	v_accvgpr_read_b32 v0, a18
	v_accvgpr_read_b32 v50, a20
	v_accvgpr_read_b32 v1, a19
	v_pk_add_f32 v[0:1], v[2:3], v[0:1]
	v_pk_add_f32 v[2:3], v[4:5], v[50:51]
	s_waitcnt vmcnt(4)
	v_pk_add_f32 v[0:1], v[6:7], v[0:1]
	v_pk_add_f32 v[2:3], v[8:9], v[2:3]
	global_store_dwordx4 v[26:27], v[10:13], off offset:64 sc1
	global_store_dwordx4 v[26:27], v[0:3], off offset:128 sc1
	s_endpgm
	.p2align	8

.LBB8_26:
	s_or_b64 exec, exec, s[0:1]
	v_lshlrev_b32_e32 v0, 3, v81
	v_lshl_or_b32 v0, v82, 9, v0
	v_add_u32_e32 v87, 0x1800, v0
	s_waitcnt lgkmcnt(0)
	s_barrier
	ds_read2_b64 v[50:53], v87 offset0:128 offset1:144
	v_or_b32_e32 v0, v1, v80
	v_lshlrev_b32_e32 v112, 2, v0
	v_lshl_add_u32 v1, v82, 6, s22
	v_or_b32_e32 v86, v1, v81
	ds_read_b128 v[70:73], v112 offset:4096
	ds_read_b128 v[76:79], v112 offset:4864
	ds_read_b128 v[80:83], v112 offset:5632
	ds_read_b128 v[88:91], v112 offset:6400
	ds_read_b128 v[92:95], v112 offset:4160
	ds_read_b128 v[96:99], v112 offset:4224
	v_add_u32_e32 v66, s18, v0
	v_mad_i64_i32 v[0:1], s[0:1], v86, s5, 0
	s_waitcnt lgkmcnt(4)
	v_pk_add_f32 v[76:77], v[70:71], v[76:77]
	v_lshl_add_u64 v[68:69], v[0:1], 1, s[16:17]
	s_waitcnt lgkmcnt(2)
	v_pk_add_f32 v[84:85], v[80:81], v[88:89]
	v_pk_fma_f32 v[0:1], v[50:51], v[76:77], v[38:39] op_sel_hi:[0,1,1] neg_lo:[1,0,0] neg_hi:[1,0,0]
	v_pk_fma_f32 v[0:1], v[50:51], v[0:1], v[84:85] op_sel:[1,0,0]
	s_mov_b32 s6, 0x3f3504f3
	v_pk_add_f32 v[0:1], v[10:11], v[0:1]
	s_mov_b32 s1, 0x3ea7ba05
	v_pk_mul_f32 v[38:39], v[0:1], s[6:7] op_sel_hi:[1,0]
	v_pk_mul_f32 v[80:81], v[0:1], 0.5 op_sel_hi:[1,0]
	v_fma_f32 v67, |v38|, s1, 1.0
	v_fma_f32 v0, |v39|, s1, 1.0
	v_rcp_f32_e32 v70, v67
	v_rcp_f32_e32 v71, v0
	v_mul_f32_e64 v67, |v38|, -|v38|
	v_mul_f32_e32 v67, 0x3fb8aa3b, v67
	s_mov_b32 s0, 0xbfba00e3
	v_exp_f32_e32 v74, v67
	s_mov_b32 s2, 0x3f87dc22
	v_mov_b64_e32 v[0:1], s[0:1]
	v_mul_f32_e64 v67, |v39|, -|v39|
	v_pk_fma_f32 v[88:89], v[70:71], s[2:3], v[0:1] op_sel_hi:[1,0,0]
	s_mov_b32 s8, 0x3fb5f0e3
	v_mul_f32_e32 v67, 0x3fb8aa3b, v67
	v_pk_fma_f32 v[88:89], v[70:71], v[88:89], s[8:9] op_sel_hi:[1,1,0]
	s_mov_b32 s0, 0xbe91a98e
	v_exp_f32_e32 v75, v67
	v_pk_fma_f32 v[88:89], v[70:71], v[88:89], s[0:1] op_sel_hi:[1,1,0]
	s_mov_b32 s4, 0x3e827906
	v_pk_fma_f32 v[88:89], v[70:71], v[88:89], s[4:5] op_sel_hi:[1,1,0]
	s_brev_b32 s3, -2
	v_pk_mul_f32 v[70:71], v[70:71], v[88:89]
	v_pk_add_f32 v[82:83], v[82:83], v[90:91]
	v_pk_fma_f32 v[70:71], v[74:75], v[70:71], 1.0 op_sel_hi:[1,1,0] neg_lo:[1,0,0] neg_hi:[1,0,0]
	ds_read_b128 v[100:103], v112 offset:5696
	ds_read_b128 v[104:107], v112 offset:5760
	v_bfi_b32 v39, s3, v71, v39
	v_bfi_b32 v38, s3, v70, v38
	v_pk_add_f32 v[38:39], v[38:39], 1.0 op_sel_hi:[1,0]
	ds_read_b128 v[88:91], v112 offset:4928
	ds_read_b128 v[108:111], v112 offset:4992
	v_pk_mul_f32 v[38:39], v[80:81], v[38:39]
	v_pk_add_f32 v[80:81], v[72:73], v[78:79]
	v_cvt_pk_f16_f32 v120, v38, v39
	v_pk_fma_f32 v[40:41], v[50:51], v[80:81], v[40:41] op_sel_hi:[0,1,1] neg_lo:[1,0,0] neg_hi:[1,0,0]
	v_pk_fma_f32 v[40:41], v[50:51], v[40:41], v[82:83] op_sel:[1,0,0]
	v_pk_fma_f32 v[54:55], v[52:53], v[76:77], v[54:55] op_sel_hi:[0,1,1] neg_lo:[1,0,0] neg_hi:[1,0,0]
	v_pk_add_f32 v[40:41], v[12:13], v[40:41]
	v_pk_fma_f32 v[54:55], v[52:53], v[54:55], v[84:85] op_sel:[1,0,0]
	v_pk_mul_f32 v[70:71], v[40:41], s[6:7] op_sel_hi:[1,0]
	v_pk_mul_f32 v[40:41], v[40:41], 0.5 op_sel_hi:[1,0]
	v_fma_f32 v39, |v70|, s1, 1.0
	v_fma_f32 v67, |v71|, s1, 1.0
	v_rcp_f32_e32 v72, v39
	v_rcp_f32_e32 v73, v67
	v_mul_f32_e64 v39, |v70|, -|v70|
	v_mul_f32_e32 v39, 0x3fb8aa3b, v39
	v_exp_f32_e32 v74, v39
	v_mul_f32_e64 v39, |v71|, -|v71|
	v_pk_fma_f32 v[78:79], v[72:73], s[2:3], v[0:1] op_sel_hi:[1,0,0]
	v_mul_f32_e32 v39, 0x3fb8aa3b, v39
	v_pk_fma_f32 v[78:79], v[72:73], v[78:79], s[8:9] op_sel_hi:[1,1,0]
	v_exp_f32_e32 v75, v39
	v_pk_fma_f32 v[78:79], v[72:73], v[78:79], s[0:1] op_sel_hi:[1,1,0]
	v_ashrrev_i32_e32 v67, 31, v66
	v_pk_fma_f32 v[78:79], v[72:73], v[78:79], s[4:5] op_sel_hi:[1,1,0]
	v_pk_add_f32 v[54:55], v[10:11], v[54:55]
	v_pk_mul_f32 v[72:73], v[72:73], v[78:79]
	v_pk_fma_f32 v[56:57], v[52:53], v[80:81], v[56:57] op_sel_hi:[0,1,1] neg_lo:[1,0,0] neg_hi:[1,0,0]
	v_pk_fma_f32 v[72:73], v[74:75], v[72:73], 1.0 op_sel_hi:[1,1,0] neg_lo:[1,0,0] neg_hi:[1,0,0]
	s_waitcnt lgkmcnt(1)
	v_pk_add_f32 v[74:75], v[92:93], v[88:89]
	v_bfi_b32 v71, s3, v73, v71
	v_bfi_b32 v70, s3, v72, v70
	v_pk_add_f32 v[70:71], v[70:71], 1.0 op_sel_hi:[1,0]
	v_lshlrev_b64 v[72:73], 1, v[66:67]
	v_pk_mul_f32 v[40:41], v[40:41], v[70:71]
	v_lshl_add_u64 v[116:117], v[68:69], 0, v[72:73]
	ds_read_b128 v[68:71], v112 offset:6464
	v_cvt_pk_f16_f32 v121, v40, v41
	v_mbcnt_lo_u32_b32 v118, -1, 0
	v_mbcnt_hi_u32_b32 v118, -1, v118
	v_bfe_u32 v137, v118, 4, 1
	v_and_b32_e32 v118, 16, v118
	v_lshrrev_b32_e32 v119, 1, v118
	v_add_u32_e32 v118, v118, v119
	v_mov_b32_e32 v119, 0
	v_mul_u32_u24_e32 v136, 0x17ff8, v137
	v_add_u32_e32 v136, 0xfffe8040, v136
	v_add_u32_e32 v137, -1, v137
	v_pk_fma_f32 v[38:39], v[50:51], v[74:75], v[62:63] op_sel_hi:[0,1,1] neg_lo:[1,0,0] neg_hi:[1,0,0]
	ds_read_b128 v[112:115], v112 offset:6528
	s_waitcnt lgkmcnt(1)
	v_pk_add_f32 v[78:79], v[100:101], v[68:69]
	v_pk_add_f32 v[70:71], v[102:103], v[70:71]
	v_pk_fma_f32 v[38:39], v[50:51], v[38:39], v[78:79] op_sel:[1,0,0]
	v_pk_fma_f32 v[56:57], v[52:53], v[56:57], v[82:83] op_sel:[1,0,0]
	v_pk_add_f32 v[62:63], v[6:7], v[38:39]
	v_pk_add_f32 v[56:57], v[12:13], v[56:57]
	v_pk_mul_f32 v[66:67], v[62:63], s[6:7] op_sel_hi:[1,0]
	v_pk_mul_f32 v[62:63], v[62:63], 0.5 op_sel_hi:[1,0]
	v_fma_f32 v38, |v66|, s1, 1.0
	v_fma_f32 v39, |v67|, s1, 1.0
	v_rcp_f32_e32 v38, v38
	v_rcp_f32_e32 v39, v39
	v_mul_f32_e64 v40, |v66|, -|v66|
	v_mul_f32_e32 v40, 0x3fb8aa3b, v40
	v_mul_f32_e64 v69, |v67|, -|v67|
	v_exp_f32_e32 v68, v40
	v_pk_fma_f32 v[40:41], v[38:39], s[2:3], v[0:1] op_sel_hi:[1,0,0]
	v_mul_f32_e32 v69, 0x3fb8aa3b, v69
	v_pk_fma_f32 v[40:41], v[38:39], v[40:41], s[8:9] op_sel_hi:[1,1,0]
	v_exp_f32_e32 v69, v69
	v_pk_fma_f32 v[40:41], v[38:39], v[40:41], s[0:1] op_sel_hi:[1,1,0]
	v_pk_fma_f32 v[46:47], v[52:53], v[74:75], v[46:47] op_sel_hi:[0,1,1] neg_lo:[1,0,0] neg_hi:[1,0,0]
	v_pk_fma_f32 v[40:41], v[38:39], v[40:41], s[4:5] op_sel_hi:[1,1,0]
	v_pk_fma_f32 v[46:47], v[52:53], v[46:47], v[78:79] op_sel:[1,0,0]
	v_pk_mul_f32 v[88:89], v[38:39], v[40:41]
	ds_read2_b64 v[38:41], v87 offset0:160 offset1:176
	v_pk_fma_f32 v[68:69], v[68:69], v[88:89], 1.0 op_sel_hi:[1,1,0] neg_lo:[1,0,0] neg_hi:[1,0,0]
	v_pk_add_f32 v[46:47], v[6:7], v[46:47]
	v_bfi_b32 v67, s3, v69, v67
	v_bfi_b32 v66, s3, v68, v66
	v_pk_add_f32 v[68:69], v[94:95], v[90:91]
	v_pk_add_f32 v[66:67], v[66:67], 1.0 op_sel_hi:[1,0]
	v_pk_fma_f32 v[64:65], v[50:51], v[68:69], v[64:65] op_sel_hi:[0,1,1] neg_lo:[1,0,0] neg_hi:[1,0,0]
	v_pk_fma_f32 v[64:65], v[50:51], v[64:65], v[70:71] op_sel:[1,0,0]
	v_pk_mul_f32 v[62:63], v[62:63], v[66:67]
	v_pk_add_f32 v[64:65], v[8:9], v[64:65]
	v_cvt_pk_f16_f32 v122, v62, v63
	v_pk_mul_f32 v[66:67], v[64:65], s[6:7] op_sel_hi:[1,0]
	v_pk_mul_f32 v[64:65], v[64:65], 0.5 op_sel_hi:[1,0]
	v_fma_f32 v63, |v66|, s1, 1.0
	v_fma_f32 v87, |v67|, s1, 1.0
	v_rcp_f32_e32 v88, v63
	v_rcp_f32_e32 v89, v87
	v_mul_f32_e64 v63, |v66|, -|v66|
	v_mul_f32_e32 v63, 0x3fb8aa3b, v63
	v_exp_f32_e32 v90, v63
	v_mul_f32_e64 v63, |v67|, -|v67|
	v_pk_fma_f32 v[92:93], v[88:89], s[2:3], v[0:1] op_sel_hi:[1,0,0]
	v_mul_f32_e32 v63, 0x3fb8aa3b, v63
	v_pk_fma_f32 v[92:93], v[88:89], v[92:93], s[8:9] op_sel_hi:[1,1,0]
	v_exp_f32_e32 v91, v63
	v_pk_fma_f32 v[92:93], v[88:89], v[92:93], s[0:1] op_sel_hi:[1,1,0]
	v_pk_fma_f32 v[48:49], v[52:53], v[68:69], v[48:49] op_sel_hi:[0,1,1] neg_lo:[1,0,0] neg_hi:[1,0,0]
	v_pk_fma_f32 v[92:93], v[88:89], v[92:93], s[4:5] op_sel_hi:[1,1,0]
	v_pk_fma_f32 v[48:49], v[52:53], v[48:49], v[70:71] op_sel:[1,0,0]
	v_pk_mul_f32 v[88:89], v[88:89], v[92:93]
	v_pk_add_f32 v[48:49], v[8:9], v[48:49]
	v_pk_fma_f32 v[88:89], v[90:91], v[88:89], 1.0 op_sel_hi:[1,1,0] neg_lo:[1,0,0] neg_hi:[1,0,0]
	s_waitcnt lgkmcnt(0)
	v_pk_fma_f32 v[34:35], v[38:39], v[76:77], v[34:35] op_sel_hi:[0,1,1] neg_lo:[1,0,0] neg_hi:[1,0,0]
	v_bfi_b32 v67, s3, v89, v67
	v_bfi_b32 v66, s3, v88, v66
	v_pk_add_f32 v[66:67], v[66:67], 1.0 op_sel_hi:[1,0]
	v_pk_fma_f32 v[34:35], v[38:39], v[34:35], v[84:85] op_sel:[1,0,0]
	v_pk_mul_f32 v[64:65], v[64:65], v[66:67]
	v_pk_add_f32 v[34:35], v[10:11], v[34:35]
	v_cvt_pk_f16_f32 v123, v64, v65
	v_lshl_add_u64 v[138:139], v[116:117], 0, v[118:119]
	s_nop 1
	v_permlane16_swap_b32 v120, v122
	v_permlane16_swap_b32 v121, v123
	global_store_dwordx4 v[138:139], v[120:123], off sc1
	v_pk_add_f32 v[62:63], v[96:97], v[108:109]
	v_pk_add_f32 v[64:65], v[104:105], v[112:113]
	v_pk_fma_f32 v[58:59], v[50:51], v[62:63], v[58:59] op_sel_hi:[0,1,1] neg_lo:[1,0,0] neg_hi:[1,0,0]
	v_pk_fma_f32 v[58:59], v[50:51], v[58:59], v[64:65] op_sel:[1,0,0]
	v_pk_fma_f32 v[42:43], v[52:53], v[62:63], v[42:43] op_sel_hi:[0,1,1] neg_lo:[1,0,0] neg_hi:[1,0,0]
	v_pk_add_f32 v[58:59], v[2:3], v[58:59]
	v_pk_fma_f32 v[42:43], v[52:53], v[42:43], v[64:65] op_sel:[1,0,0]
	v_pk_mul_f32 v[66:67], v[58:59], s[6:7] op_sel_hi:[1,0]
	v_pk_mul_f32 v[58:59], v[58:59], 0.5 op_sel_hi:[1,0]
	v_fma_f32 v87, |v66|, s1, 1.0
	v_fma_f32 v89, |v67|, s1, 1.0
	v_rcp_f32_e32 v88, v87
	v_rcp_f32_e32 v89, v89
	v_mul_f32_e64 v87, |v66|, -|v66|
	v_mul_f32_e32 v87, 0x3fb8aa3b, v87
	v_exp_f32_e32 v90, v87
	v_mul_f32_e64 v87, |v67|, -|v67|
	v_pk_fma_f32 v[92:93], v[88:89], s[2:3], v[0:1] op_sel_hi:[1,0,0]
	v_mul_f32_e32 v87, 0x3fb8aa3b, v87
	v_pk_fma_f32 v[92:93], v[88:89], v[92:93], s[8:9] op_sel_hi:[1,1,0]
	v_exp_f32_e32 v91, v87
	v_pk_fma_f32 v[92:93], v[88:89], v[92:93], s[0:1] op_sel_hi:[1,1,0]
	v_pk_add_f32 v[42:43], v[2:3], v[42:43]
	v_pk_fma_f32 v[92:93], v[88:89], v[92:93], s[4:5] op_sel_hi:[1,1,0]
	v_pk_fma_f32 v[36:37], v[38:39], v[80:81], v[36:37] op_sel_hi:[0,1,1] neg_lo:[1,0,0] neg_hi:[1,0,0]
	v_pk_mul_f32 v[88:89], v[88:89], v[92:93]
	v_pk_fma_f32 v[36:37], v[38:39], v[36:37], v[82:83] op_sel:[1,0,0]
	v_pk_fma_f32 v[88:89], v[90:91], v[88:89], 1.0 op_sel_hi:[1,1,0] neg_lo:[1,0,0] neg_hi:[1,0,0]
	v_pk_add_f32 v[36:37], v[12:13], v[36:37]
	v_bfi_b32 v67, s3, v89, v67
	v_bfi_b32 v66, s3, v88, v66
	v_pk_add_f32 v[66:67], v[66:67], 1.0 op_sel_hi:[1,0]
	v_pk_fma_f32 v[30:31], v[38:39], v[74:75], v[30:31] op_sel_hi:[0,1,1] neg_lo:[1,0,0] neg_hi:[1,0,0]
	v_pk_mul_f32 v[58:59], v[58:59], v[66:67]
	v_pk_add_f32 v[66:67], v[106:107], v[114:115]
	v_cvt_pk_f16_f32 v128, v58, v59
	v_pk_add_f32 v[58:59], v[98:99], v[110:111]
	v_pk_fma_f32 v[30:31], v[38:39], v[30:31], v[78:79] op_sel:[1,0,0]
	v_pk_fma_f32 v[60:61], v[50:51], v[58:59], v[60:61] op_sel_hi:[0,1,1] neg_lo:[1,0,0] neg_hi:[1,0,0]
	v_pk_fma_f32 v[50:51], v[50:51], v[60:61], v[66:67] op_sel:[1,0,0]
	v_pk_fma_f32 v[44:45], v[52:53], v[58:59], v[44:45] op_sel_hi:[0,1,1] neg_lo:[1,0,0] neg_hi:[1,0,0]
	v_pk_add_f32 v[50:51], v[4:5], v[50:51]
	v_pk_fma_f32 v[44:45], v[52:53], v[44:45], v[66:67] op_sel:[1,0,0]
	v_pk_mul_f32 v[60:61], v[50:51], s[6:7] op_sel_hi:[1,0]
	v_pk_mul_f32 v[50:51], v[50:51], 0.5 op_sel_hi:[1,0]
	v_fma_f32 v87, |v60|, s1, 1.0
	v_fma_f32 v89, |v61|, s1, 1.0
	v_rcp_f32_e32 v90, v87
	v_rcp_f32_e32 v91, v89
	v_mul_f32_e64 v87, |v60|, -|v60|
	v_mul_f32_e32 v87, 0x3fb8aa3b, v87
	v_exp_f32_e32 v92, v87
	v_mul_f32_e64 v87, |v61|, -|v61|
	v_pk_fma_f32 v[94:95], v[90:91], s[2:3], v[0:1] op_sel_hi:[1,0,0]
	v_mul_f32_e32 v87, 0x3fb8aa3b, v87
	v_pk_fma_f32 v[94:95], v[90:91], v[94:95], s[8:9] op_sel_hi:[1,1,0]
	v_exp_f32_e32 v93, v87
	v_pk_fma_f32 v[94:95], v[90:91], v[94:95], s[0:1] op_sel_hi:[1,1,0]
	v_pk_add_f32 v[44:45], v[4:5], v[44:45]
	v_pk_fma_f32 v[94:95], v[90:91], v[94:95], s[4:5] op_sel_hi:[1,1,0]
	v_pk_add_f32 v[30:31], v[6:7], v[30:31]
	v_pk_mul_f32 v[90:91], v[90:91], v[94:95]
	v_pk_fma_f32 v[32:33], v[38:39], v[68:69], v[32:33] op_sel_hi:[0,1,1] neg_lo:[1,0,0] neg_hi:[1,0,0]
	v_pk_fma_f32 v[90:91], v[92:93], v[90:91], 1.0 op_sel_hi:[1,1,0] neg_lo:[1,0,0] neg_hi:[1,0,0]
	v_pk_fma_f32 v[32:33], v[38:39], v[32:33], v[70:71] op_sel:[1,0,0]
	v_bfi_b32 v61, s3, v91, v61
	v_bfi_b32 v60, s3, v90, v60
	v_pk_add_f32 v[60:61], v[60:61], 1.0 op_sel_hi:[1,0]
	v_pk_add_f32 v[32:33], v[8:9], v[32:33]
	v_pk_mul_f32 v[50:51], v[50:51], v[60:61]
	v_pk_mul_f32 v[60:61], v[54:55], s[6:7] op_sel_hi:[1,0]
	v_cvt_pk_f16_f32 v129, v50, v51
	v_fma_f32 v87, |v60|, s1, 1.0
	v_fma_f32 v89, |v61|, s1, 1.0
	v_rcp_f32_e32 v88, v87
	v_rcp_f32_e32 v89, v89
	v_mul_f32_e64 v87, |v60|, -|v60|
	v_mul_f32_e32 v87, 0x3fb8aa3b, v87
	v_exp_f32_e32 v90, v87
	v_mul_f32_e64 v87, |v61|, -|v61|
	v_pk_fma_f32 v[92:93], v[88:89], s[2:3], v[0:1] op_sel_hi:[1,0,0]
	v_mul_f32_e32 v87, 0x3fb8aa3b, v87
	v_pk_fma_f32 v[92:93], v[88:89], v[92:93], s[8:9] op_sel_hi:[1,1,0]
	v_exp_f32_e32 v91, v87
	v_pk_fma_f32 v[92:93], v[88:89], v[92:93], s[0:1] op_sel_hi:[1,1,0]
	v_pk_mul_f32 v[54:55], v[54:55], 0.5 op_sel_hi:[1,0]
	v_pk_fma_f32 v[92:93], v[88:89], v[92:93], s[4:5] op_sel_hi:[1,1,0]
	v_or_b32_e32 v50, 16, v86
	v_pk_mul_f32 v[88:89], v[88:89], v[92:93]
	v_mad_i64_i32 v[50:51], s[10:11], v50, s5, 0
	v_pk_fma_f32 v[88:89], v[90:91], v[88:89], 1.0 op_sel_hi:[1,1,0] neg_lo:[1,0,0] neg_hi:[1,0,0]
	v_lshl_add_u64 v[50:51], v[50:51], 1, s[16:17]
	v_bfi_b32 v61, s3, v89, v61
	v_bfi_b32 v60, s3, v88, v60
	v_pk_add_f32 v[60:61], v[60:61], 1.0 op_sel_hi:[1,0]
	v_lshl_add_u64 v[50:51], v[50:51], 0, v[72:73]
	v_pk_mul_f32 v[54:55], v[54:55], v[60:61]
	v_pk_mul_f32 v[60:61], v[56:57], s[6:7] op_sel_hi:[1,0]
	v_cvt_pk_f16_f32 v124, v54, v55
	v_fma_f32 v55, |v60|, s1, 1.0
	v_fma_f32 v87, |v61|, s1, 1.0
	v_rcp_f32_e32 v88, v55
	v_rcp_f32_e32 v89, v87
	v_mul_f32_e64 v55, |v60|, -|v60|
	v_mul_f32_e32 v55, 0x3fb8aa3b, v55
	v_exp_f32_e32 v90, v55
	v_mul_f32_e64 v55, |v61|, -|v61|
	v_pk_fma_f32 v[92:93], v[88:89], s[2:3], v[0:1] op_sel_hi:[1,0,0]
	v_mul_f32_e32 v55, 0x3fb8aa3b, v55
	v_pk_fma_f32 v[92:93], v[88:89], v[92:93], s[8:9] op_sel_hi:[1,1,0]
	v_exp_f32_e32 v91, v55
	v_pk_fma_f32 v[92:93], v[88:89], v[92:93], s[0:1] op_sel_hi:[1,1,0]
	v_pk_mul_f32 v[56:57], v[56:57], 0.5 op_sel_hi:[1,0]
	v_pk_fma_f32 v[92:93], v[88:89], v[92:93], s[4:5] op_sel_hi:[1,1,0]
	v_pk_fma_f32 v[26:27], v[38:39], v[62:63], v[26:27] op_sel_hi:[0,1,1] neg_lo:[1,0,0] neg_hi:[1,0,0]
	v_pk_mul_f32 v[88:89], v[88:89], v[92:93]
	v_pk_fma_f32 v[26:27], v[38:39], v[26:27], v[64:65] op_sel:[1,0,0]
	v_pk_fma_f32 v[88:89], v[90:91], v[88:89], 1.0 op_sel_hi:[1,1,0] neg_lo:[1,0,0] neg_hi:[1,0,0]
	v_pk_add_f32 v[26:27], v[2:3], v[26:27]
	v_bfi_b32 v61, s3, v89, v61
	v_bfi_b32 v60, s3, v88, v60
	v_pk_add_f32 v[60:61], v[60:61], 1.0 op_sel_hi:[1,0]
	v_pk_fma_f32 v[28:29], v[38:39], v[58:59], v[28:29] op_sel_hi:[0,1,1] neg_lo:[1,0,0] neg_hi:[1,0,0]
	v_pk_mul_f32 v[56:57], v[56:57], v[60:61]
	v_pk_fma_f32 v[28:29], v[38:39], v[28:29], v[66:67] op_sel:[1,0,0]
	v_cvt_pk_f16_f32 v125, v56, v57
	v_pk_mul_f32 v[54:55], v[46:47], s[6:7] op_sel_hi:[1,0]
	v_pk_mul_f32 v[46:47], v[46:47], 0.5 op_sel_hi:[1,0]
	v_fma_f32 v56, |v54|, s1, 1.0
	v_fma_f32 v57, |v55|, s1, 1.0
	v_rcp_f32_e32 v56, v56
	v_rcp_f32_e32 v57, v57
	v_mul_f32_e64 v60, |v54|, -|v54|
	v_mul_f32_e64 v61, |v55|, -|v55|
	v_mul_f32_e32 v60, 0x3fb8aa3b, v60
	v_pk_fma_f32 v[88:89], v[56:57], s[2:3], v[0:1] op_sel_hi:[1,0,0]
	v_mul_f32_e32 v61, 0x3fb8aa3b, v61
	v_exp_f32_e32 v60, v60
	v_pk_fma_f32 v[88:89], v[56:57], v[88:89], s[8:9] op_sel_hi:[1,1,0]
	v_exp_f32_e32 v61, v61
	v_pk_fma_f32 v[88:89], v[56:57], v[88:89], s[0:1] op_sel_hi:[1,1,0]
	v_pk_add_f32 v[28:29], v[4:5], v[28:29]
	v_pk_fma_f32 v[88:89], v[56:57], v[88:89], s[4:5] op_sel_hi:[1,1,0]
	v_pk_fma_f32 v[22:23], v[40:41], v[76:77], v[22:23] op_sel_hi:[0,1,1] neg_lo:[1,0,0] neg_hi:[1,0,0]
	v_pk_mul_f32 v[56:57], v[56:57], v[88:89]
	v_pk_fma_f32 v[22:23], v[40:41], v[22:23], v[84:85] op_sel:[1,0,0]
	v_pk_fma_f32 v[56:57], v[60:61], v[56:57], 1.0 op_sel_hi:[1,1,0] neg_lo:[1,0,0] neg_hi:[1,0,0]
	v_pk_add_f32 v[10:11], v[10:11], v[22:23]
	v_bfi_b32 v55, s3, v57, v55
	v_bfi_b32 v54, s3, v56, v54
	v_pk_add_f32 v[54:55], v[54:55], 1.0 op_sel_hi:[1,0]
	v_pk_mul_f32 v[22:23], v[10:11], s[6:7] op_sel_hi:[1,0]
	v_pk_mul_f32 v[46:47], v[46:47], v[54:55]
	v_pk_mul_f32 v[54:55], v[48:49], s[6:7] op_sel_hi:[1,0]
	v_cvt_pk_f16_f32 v126, v46, v47
	v_fma_f32 v47, |v54|, s1, 1.0
	v_fma_f32 v57, |v55|, s1, 1.0
	v_rcp_f32_e32 v56, v47
	v_rcp_f32_e32 v57, v57
	v_mul_f32_e64 v47, |v54|, -|v54|
	v_mul_f32_e32 v47, 0x3fb8aa3b, v47
	v_exp_f32_e32 v60, v47
	v_mul_f32_e64 v47, |v55|, -|v55|
	v_pk_fma_f32 v[88:89], v[56:57], s[2:3], v[0:1] op_sel_hi:[1,0,0]
	v_mul_f32_e32 v47, 0x3fb8aa3b, v47
	v_pk_fma_f32 v[88:89], v[56:57], v[88:89], s[8:9] op_sel_hi:[1,1,0]
	v_exp_f32_e32 v61, v47
	v_pk_fma_f32 v[88:89], v[56:57], v[88:89], s[0:1] op_sel_hi:[1,1,0]
	v_pk_mul_f32 v[48:49], v[48:49], 0.5 op_sel_hi:[1,0]
	v_pk_fma_f32 v[88:89], v[56:57], v[88:89], s[4:5] op_sel_hi:[1,1,0]
	v_pk_mul_f32 v[10:11], v[10:11], 0.5 op_sel_hi:[1,0]
	v_pk_mul_f32 v[56:57], v[56:57], v[88:89]
	s_nop 0
	v_pk_fma_f32 v[56:57], v[60:61], v[56:57], 1.0 op_sel_hi:[1,1,0] neg_lo:[1,0,0] neg_hi:[1,0,0]
	s_nop 0
	v_bfi_b32 v55, s3, v57, v55
	v_bfi_b32 v54, s3, v56, v54
	v_pk_add_f32 v[54:55], v[54:55], 1.0 op_sel_hi:[1,0]
	s_nop 0
	v_pk_mul_f32 v[48:49], v[48:49], v[54:55]
	s_nop 0
	v_cvt_pk_f16_f32 v127, v48, v49
	v_lshl_add_u64 v[138:139], v[50:51], 0, v[118:119]
	s_nop 1
	v_permlane16_swap_b32 v124, v126
	v_permlane16_swap_b32 v125, v127
	global_store_dwordx4 v[138:139], v[124:127], off sc1
	v_pk_mul_f32 v[46:47], v[42:43], s[6:7] op_sel_hi:[1,0]
	v_pk_mul_f32 v[42:43], v[42:43], 0.5 op_sel_hi:[1,0]
	v_fma_f32 v48, |v46|, s1, 1.0
	v_fma_f32 v49, |v47|, s1, 1.0
	v_rcp_f32_e32 v48, v48
	v_rcp_f32_e32 v49, v49
	v_mul_f32_e64 v54, |v46|, -|v46|
	v_mul_f32_e64 v55, |v47|, -|v47|
	v_mul_f32_e32 v54, 0x3fb8aa3b, v54
	v_pk_fma_f32 v[56:57], v[48:49], s[2:3], v[0:1] op_sel_hi:[1,0,0]
	v_mul_f32_e32 v55, 0x3fb8aa3b, v55
	v_exp_f32_e32 v54, v54
	v_pk_fma_f32 v[56:57], v[48:49], v[56:57], s[8:9] op_sel_hi:[1,1,0]
	v_exp_f32_e32 v55, v55
	v_pk_fma_f32 v[56:57], v[48:49], v[56:57], s[0:1] op_sel_hi:[1,1,0]
	s_nop 0
	v_pk_fma_f32 v[56:57], v[48:49], v[56:57], s[4:5] op_sel_hi:[1,1,0]
	s_nop 0
	v_pk_mul_f32 v[48:49], v[48:49], v[56:57]
	s_nop 0
	v_pk_fma_f32 v[48:49], v[54:55], v[48:49], 1.0 op_sel_hi:[1,1,0] neg_lo:[1,0,0] neg_hi:[1,0,0]
	s_nop 0
	v_bfi_b32 v47, s3, v49, v47
	v_bfi_b32 v46, s3, v48, v46
	v_pk_add_f32 v[46:47], v[46:47], 1.0 op_sel_hi:[1,0]
	s_nop 0
	v_pk_mul_f32 v[42:43], v[42:43], v[46:47]
	v_pk_mul_f32 v[46:47], v[44:45], s[6:7] op_sel_hi:[1,0]
	v_cvt_pk_f16_f32 v130, v42, v43
	v_fma_f32 v43, |v46|, s1, 1.0
	v_fma_f32 v49, |v47|, s1, 1.0
	v_rcp_f32_e32 v48, v43
	v_rcp_f32_e32 v49, v49
	v_mul_f32_e64 v43, |v46|, -|v46|
	v_mul_f32_e32 v43, 0x3fb8aa3b, v43
	v_exp_f32_e32 v52, v43
	v_mul_f32_e64 v43, |v47|, -|v47|
	v_pk_fma_f32 v[54:55], v[48:49], s[2:3], v[0:1] op_sel_hi:[1,0,0]
	v_mul_f32_e32 v43, 0x3fb8aa3b, v43
	v_pk_fma_f32 v[54:55], v[48:49], v[54:55], s[8:9] op_sel_hi:[1,1,0]
	v_exp_f32_e32 v53, v43
	v_pk_fma_f32 v[54:55], v[48:49], v[54:55], s[0:1] op_sel_hi:[1,1,0]
	v_pk_mul_f32 v[44:45], v[44:45], 0.5 op_sel_hi:[1,0]
	v_pk_fma_f32 v[54:55], v[48:49], v[54:55], s[4:5] op_sel_hi:[1,1,0]
	s_nop 0
	v_pk_mul_f32 v[48:49], v[48:49], v[54:55]
	s_nop 0
	v_pk_fma_f32 v[48:49], v[52:53], v[48:49], 1.0 op_sel_hi:[1,1,0] neg_lo:[1,0,0] neg_hi:[1,0,0]
	s_nop 0
	v_bfi_b32 v47, s3, v49, v47
	v_bfi_b32 v46, s3, v48, v46
	v_pk_add_f32 v[46:47], v[46:47], 1.0 op_sel_hi:[1,0]
	s_nop 0
	v_pk_mul_f32 v[44:45], v[44:45], v[46:47]
	s_nop 0
	v_cvt_pk_f16_f32 v131, v44, v45
	v_pk_mul_f32 v[44:45], v[34:35], s[6:7] op_sel_hi:[1,0]
	v_lshl_add_u64 v[138:139], v[50:51], 0, v[136:137]
	s_nop 1
	v_permlane16_swap_b32 v128, v130
	v_permlane16_swap_b32 v129, v131
	global_store_dwordx4 v[138:139], v[128:131], off sc1
	v_fma_f32 v46, |v44|, s1, 1.0
	v_fma_f32 v47, |v45|, s1, 1.0
	v_rcp_f32_e32 v46, v46
	v_rcp_f32_e32 v47, v47
	v_mul_f32_e64 v48, |v44|, -|v44|
	v_mul_f32_e64 v49, |v45|, -|v45|
	v_mul_f32_e32 v48, 0x3fb8aa3b, v48
	v_pk_fma_f32 v[50:51], v[46:47], s[2:3], v[0:1] op_sel_hi:[1,0,0]
	v_mul_f32_e32 v49, 0x3fb8aa3b, v49
	v_exp_f32_e32 v48, v48
	v_pk_fma_f32 v[50:51], v[46:47], v[50:51], s[8:9] op_sel_hi:[1,1,0]
	v_exp_f32_e32 v49, v49
	v_pk_fma_f32 v[50:51], v[46:47], v[50:51], s[0:1] op_sel_hi:[1,1,0]
	v_pk_mul_f32 v[34:35], v[34:35], 0.5 op_sel_hi:[1,0]
	v_pk_fma_f32 v[50:51], v[46:47], v[50:51], s[4:5] op_sel_hi:[1,1,0]
	v_or_b32_e32 v42, 32, v86
	v_pk_mul_f32 v[46:47], v[46:47], v[50:51]
	v_mad_i64_i32 v[42:43], s[10:11], v42, s5, 0
	v_pk_fma_f32 v[46:47], v[48:49], v[46:47], 1.0 op_sel_hi:[1,1,0] neg_lo:[1,0,0] neg_hi:[1,0,0]
	v_lshl_add_u64 v[42:43], v[42:43], 1, s[16:17]
	v_bfi_b32 v45, s3, v47, v45
	v_bfi_b32 v44, s3, v46, v44
	v_pk_add_f32 v[44:45], v[44:45], 1.0 op_sel_hi:[1,0]
	s_nop 0
	v_pk_mul_f32 v[34:35], v[34:35], v[44:45]
	v_pk_mul_f32 v[44:45], v[36:37], s[6:7] op_sel_hi:[1,0]
	v_cvt_pk_f16_f32 v120, v34, v35
	v_fma_f32 v35, |v44|, s1, 1.0
	v_fma_f32 v47, |v45|, s1, 1.0
	v_rcp_f32_e32 v46, v35
	v_rcp_f32_e32 v47, v47
	v_mul_f32_e64 v35, |v44|, -|v44|
	v_mul_f32_e32 v35, 0x3fb8aa3b, v35
	v_exp_f32_e32 v48, v35
	v_mul_f32_e64 v35, |v45|, -|v45|
	v_pk_fma_f32 v[50:51], v[46:47], s[2:3], v[0:1] op_sel_hi:[1,0,0]
	v_mul_f32_e32 v35, 0x3fb8aa3b, v35
	v_pk_fma_f32 v[50:51], v[46:47], v[50:51], s[8:9] op_sel_hi:[1,1,0]
	v_exp_f32_e32 v49, v35
	v_pk_fma_f32 v[50:51], v[46:47], v[50:51], s[0:1] op_sel_hi:[1,1,0]
	v_pk_mul_f32 v[36:37], v[36:37], 0.5 op_sel_hi:[1,0]
	v_pk_fma_f32 v[50:51], v[46:47], v[50:51], s[4:5] op_sel_hi:[1,1,0]
	s_nop 0
	v_pk_mul_f32 v[46:47], v[46:47], v[50:51]
	s_nop 0
	v_pk_fma_f32 v[46:47], v[48:49], v[46:47], 1.0 op_sel_hi:[1,1,0] neg_lo:[1,0,0] neg_hi:[1,0,0]
	s_nop 0
	v_bfi_b32 v45, s3, v47, v45
	v_bfi_b32 v44, s3, v46, v44
	v_pk_add_f32 v[44:45], v[44:45], 1.0 op_sel_hi:[1,0]
	s_nop 0
	v_pk_mul_f32 v[36:37], v[36:37], v[44:45]
	s_nop 0
	v_cvt_pk_f16_f32 v121, v36, v37
	v_lshl_add_u64 v[36:37], v[42:43], 0, v[72:73]
	v_pk_mul_f32 v[34:35], v[30:31], s[6:7] op_sel_hi:[1,0]
	v_pk_mul_f32 v[30:31], v[30:31], 0.5 op_sel_hi:[1,0]
	v_fma_f32 v42, |v34|, s1, 1.0
	v_fma_f32 v43, |v35|, s1, 1.0
	v_rcp_f32_e32 v42, v42
	v_rcp_f32_e32 v43, v43
	v_mul_f32_e64 v44, |v34|, -|v34|
	v_mul_f32_e64 v45, |v35|, -|v35|
	v_mul_f32_e32 v44, 0x3fb8aa3b, v44
	v_pk_fma_f32 v[46:47], v[42:43], s[2:3], v[0:1] op_sel_hi:[1,0,0]
	v_mul_f32_e32 v45, 0x3fb8aa3b, v45
	v_exp_f32_e32 v44, v44
	v_pk_fma_f32 v[46:47], v[42:43], v[46:47], s[8:9] op_sel_hi:[1,1,0]
	v_exp_f32_e32 v45, v45
	v_pk_fma_f32 v[46:47], v[42:43], v[46:47], s[0:1] op_sel_hi:[1,1,0]
	s_nop 0
	v_pk_fma_f32 v[46:47], v[42:43], v[46:47], s[4:5] op_sel_hi:[1,1,0]
	s_nop 0
	v_pk_mul_f32 v[42:43], v[42:43], v[46:47]
	s_nop 0
	v_pk_fma_f32 v[42:43], v[44:45], v[42:43], 1.0 op_sel_hi:[1,1,0] neg_lo:[1,0,0] neg_hi:[1,0,0]
	s_nop 0
	v_bfi_b32 v35, s3, v43, v35
	v_bfi_b32 v34, s3, v42, v34
	v_pk_add_f32 v[34:35], v[34:35], 1.0 op_sel_hi:[1,0]
	s_nop 0
	v_pk_mul_f32 v[30:31], v[30:31], v[34:35]
	v_pk_mul_f32 v[34:35], v[32:33], s[6:7] op_sel_hi:[1,0]
	v_cvt_pk_f16_f32 v122, v30, v31
	v_fma_f32 v31, |v34|, s1, 1.0
	v_fma_f32 v43, |v35|, s1, 1.0
	v_rcp_f32_e32 v42, v31
	v_rcp_f32_e32 v43, v43
	v_mul_f32_e64 v31, |v34|, -|v34|
	v_mul_f32_e32 v31, 0x3fb8aa3b, v31
	v_exp_f32_e32 v44, v31
	v_mul_f32_e64 v31, |v35|, -|v35|
	v_pk_fma_f32 v[46:47], v[42:43], s[2:3], v[0:1] op_sel_hi:[1,0,0]
	v_mul_f32_e32 v31, 0x3fb8aa3b, v31
	v_pk_fma_f32 v[46:47], v[42:43], v[46:47], s[8:9] op_sel_hi:[1,1,0]
	v_exp_f32_e32 v45, v31
	v_pk_fma_f32 v[46:47], v[42:43], v[46:47], s[0:1] op_sel_hi:[1,1,0]
	v_pk_mul_f32 v[32:33], v[32:33], 0.5 op_sel_hi:[1,0]
	v_pk_fma_f32 v[46:47], v[42:43], v[46:47], s[4:5] op_sel_hi:[1,1,0]
	s_nop 0
	v_pk_mul_f32 v[42:43], v[42:43], v[46:47]
	s_nop 0
	v_pk_fma_f32 v[42:43], v[44:45], v[42:43], 1.0 op_sel_hi:[1,1,0] neg_lo:[1,0,0] neg_hi:[1,0,0]
	s_nop 0
	v_bfi_b32 v35, s3, v43, v35
	v_bfi_b32 v34, s3, v42, v34
	v_pk_add_f32 v[34:35], v[34:35], 1.0 op_sel_hi:[1,0]
	s_nop 0
	v_pk_mul_f32 v[32:33], v[32:33], v[34:35]
	s_nop 0
	v_cvt_pk_f16_f32 v123, v32, v33
	v_lshl_add_u64 v[138:139], v[36:37], 0, v[118:119]
	s_nop 1
	v_permlane16_swap_b32 v120, v122
	v_permlane16_swap_b32 v121, v123
	global_store_dwordx4 v[138:139], v[120:123], off sc1
	v_pk_mul_f32 v[30:31], v[26:27], s[6:7] op_sel_hi:[1,0]
	v_pk_mul_f32 v[26:27], v[26:27], 0.5 op_sel_hi:[1,0]
	v_fma_f32 v32, |v30|, s1, 1.0
	v_fma_f32 v33, |v31|, s1, 1.0
	v_rcp_f32_e32 v32, v32
	v_rcp_f32_e32 v33, v33
	v_mul_f32_e64 v34, |v30|, -|v30|
	v_mul_f32_e64 v35, |v31|, -|v31|
	v_mul_f32_e32 v34, 0x3fb8aa3b, v34
	v_pk_fma_f32 v[42:43], v[32:33], s[2:3], v[0:1] op_sel_hi:[1,0,0]
	v_mul_f32_e32 v35, 0x3fb8aa3b, v35
	v_exp_f32_e32 v34, v34
	v_pk_fma_f32 v[42:43], v[32:33], v[42:43], s[8:9] op_sel_hi:[1,1,0]
	v_exp_f32_e32 v35, v35
	v_pk_fma_f32 v[42:43], v[32:33], v[42:43], s[0:1] op_sel_hi:[1,1,0]
	s_nop 0
	v_pk_fma_f32 v[42:43], v[32:33], v[42:43], s[4:5] op_sel_hi:[1,1,0]
	s_nop 0
	v_pk_mul_f32 v[32:33], v[32:33], v[42:43]
	s_nop 0
	v_pk_fma_f32 v[32:33], v[34:35], v[32:33], 1.0 op_sel_hi:[1,1,0] neg_lo:[1,0,0] neg_hi:[1,0,0]
	s_nop 0
	v_bfi_b32 v31, s3, v33, v31
	v_bfi_b32 v30, s3, v32, v30
	v_pk_add_f32 v[30:31], v[30:31], 1.0 op_sel_hi:[1,0]
	s_nop 0
	v_pk_mul_f32 v[26:27], v[26:27], v[30:31]
	v_pk_mul_f32 v[30:31], v[28:29], s[6:7] op_sel_hi:[1,0]
	v_cvt_pk_f16_f32 v132, v26, v27
	v_fma_f32 v27, |v30|, s1, 1.0
	v_fma_f32 v33, |v31|, s1, 1.0
	v_rcp_f32_e32 v32, v27
	v_rcp_f32_e32 v33, v33
	v_mul_f32_e64 v27, |v30|, -|v30|
	v_mul_f32_e32 v27, 0x3fb8aa3b, v27
	v_exp_f32_e32 v34, v27
	v_mul_f32_e64 v27, |v31|, -|v31|
	v_pk_fma_f32 v[38:39], v[32:33], s[2:3], v[0:1] op_sel_hi:[1,0,0]
	v_mul_f32_e32 v27, 0x3fb8aa3b, v27
	v_pk_fma_f32 v[38:39], v[32:33], v[38:39], s[8:9] op_sel_hi:[1,1,0]
	v_exp_f32_e32 v35, v27
	v_pk_fma_f32 v[38:39], v[32:33], v[38:39], s[0:1] op_sel_hi:[1,1,0]
	v_pk_mul_f32 v[28:29], v[28:29], 0.5 op_sel_hi:[1,0]
	v_pk_fma_f32 v[38:39], v[32:33], v[38:39], s[4:5] op_sel_hi:[1,1,0]
	s_nop 0
	v_pk_mul_f32 v[32:33], v[32:33], v[38:39]
	s_nop 0
	v_pk_fma_f32 v[32:33], v[34:35], v[32:33], 1.0 op_sel_hi:[1,1,0] neg_lo:[1,0,0] neg_hi:[1,0,0]
	s_nop 0
	v_bfi_b32 v31, s3, v33, v31
	v_bfi_b32 v30, s3, v32, v30
	v_pk_add_f32 v[30:31], v[30:31], 1.0 op_sel_hi:[1,0]
	s_nop 0
	v_pk_mul_f32 v[28:29], v[28:29], v[30:31]
	v_mul_f32_e64 v30, |v22|, -|v22|
	v_cvt_pk_f16_f32 v133, v28, v29
	v_fma_f32 v28, |v22|, s1, 1.0
	v_fma_f32 v29, |v23|, s1, 1.0
	v_rcp_f32_e32 v28, v28
	v_rcp_f32_e32 v29, v29
	v_mul_f32_e64 v31, |v23|, -|v23|
	v_mul_f32_e32 v30, 0x3fb8aa3b, v30
	v_mul_f32_e32 v31, 0x3fb8aa3b, v31
	v_pk_fma_f32 v[32:33], v[28:29], s[2:3], v[0:1] op_sel_hi:[1,0,0]
	v_exp_f32_e32 v30, v30
	v_pk_fma_f32 v[32:33], v[28:29], v[32:33], s[8:9] op_sel_hi:[1,1,0]
	v_exp_f32_e32 v31, v31
	v_pk_fma_f32 v[32:33], v[28:29], v[32:33], s[0:1] op_sel_hi:[1,1,0]
	v_pk_fma_f32 v[32:33], v[28:29], v[32:33], s[4:5] op_sel_hi:[1,1,0]
	v_or_b32_e32 v26, 48, v86
	v_pk_mul_f32 v[28:29], v[28:29], v[32:33]
	v_mad_i64_i32 v[26:27], s[10:11], v26, s5, 0
	v_pk_fma_f32 v[28:29], v[30:31], v[28:29], 1.0 op_sel_hi:[1,1,0] neg_lo:[1,0,0] neg_hi:[1,0,0]
	v_lshl_add_u64 v[26:27], v[26:27], 1, s[16:17]
	v_bfi_b32 v23, s3, v29, v23
	v_bfi_b32 v22, s3, v28, v22
	v_pk_add_f32 v[22:23], v[22:23], 1.0 op_sel_hi:[1,0]
	s_nop 0
	v_pk_mul_f32 v[10:11], v[10:11], v[22:23]
	v_pk_fma_f32 v[22:23], v[40:41], v[80:81], v[24:25] op_sel_hi:[0,1,1] neg_lo:[1,0,0] neg_hi:[1,0,0]
	v_pk_fma_f32 v[22:23], v[40:41], v[22:23], v[82:83] op_sel:[1,0,0]
	v_cvt_pk_f16_f32 v124, v10, v11
	v_pk_add_f32 v[12:13], v[12:13], v[22:23]
	s_nop 0
	v_pk_mul_f32 v[22:23], v[12:13], s[6:7] op_sel_hi:[1,0]
	v_pk_mul_f32 v[12:13], v[12:13], 0.5 op_sel_hi:[1,0]
	v_fma_f32 v11, |v22|, s1, 1.0
	v_fma_f32 v25, |v23|, s1, 1.0
	v_rcp_f32_e32 v24, v11
	v_rcp_f32_e32 v25, v25
	v_mul_f32_e64 v11, |v22|, -|v22|
	v_mul_f32_e32 v11, 0x3fb8aa3b, v11
	v_exp_f32_e32 v28, v11
	v_mul_f32_e64 v11, |v23|, -|v23|
	v_pk_fma_f32 v[30:31], v[24:25], s[2:3], v[0:1] op_sel_hi:[1,0,0]
	v_mul_f32_e32 v11, 0x3fb8aa3b, v11
	v_pk_fma_f32 v[30:31], v[24:25], v[30:31], s[8:9] op_sel_hi:[1,1,0]
	v_exp_f32_e32 v29, v11
	v_pk_fma_f32 v[30:31], v[24:25], v[30:31], s[0:1] op_sel_hi:[1,1,0]
	s_nop 0
	v_pk_fma_f32 v[30:31], v[24:25], v[30:31], s[4:5] op_sel_hi:[1,1,0]
	s_nop 0
	v_pk_mul_f32 v[24:25], v[24:25], v[30:31]
	s_nop 0
	v_pk_fma_f32 v[24:25], v[28:29], v[24:25], 1.0 op_sel_hi:[1,1,0] neg_lo:[1,0,0] neg_hi:[1,0,0]
	s_nop 0
	v_bfi_b32 v23, s3, v25, v23
	v_bfi_b32 v22, s3, v24, v22
	v_pk_add_f32 v[22:23], v[22:23], 1.0 op_sel_hi:[1,0]
	s_nop 0
	v_pk_mul_f32 v[12:13], v[12:13], v[22:23]
	s_nop 0
	v_cvt_pk_f16_f32 v125, v12, v13
	v_lshl_add_u64 v[12:13], v[26:27], 0, v[72:73]
	v_pk_fma_f32 v[10:11], v[40:41], v[74:75], v[18:19] op_sel_hi:[0,1,1] neg_lo:[1,0,0] neg_hi:[1,0,0]
	v_pk_fma_f32 v[10:11], v[40:41], v[10:11], v[78:79] op_sel:[1,0,0]
	s_nop 0
	v_pk_add_f32 v[6:7], v[6:7], v[10:11]
	s_nop 0
	v_pk_mul_f32 v[10:11], v[6:7], s[6:7] op_sel_hi:[1,0]
	v_pk_mul_f32 v[6:7], v[6:7], 0.5 op_sel_hi:[1,0]
	v_fma_f32 v18, |v10|, s1, 1.0
	v_fma_f32 v19, |v11|, s1, 1.0
	v_rcp_f32_e32 v18, v18
	v_rcp_f32_e32 v19, v19
	v_mul_f32_e64 v22, |v10|, -|v10|
	v_mul_f32_e64 v23, |v11|, -|v11|
	v_mul_f32_e32 v22, 0x3fb8aa3b, v22
	v_pk_fma_f32 v[24:25], v[18:19], s[2:3], v[0:1] op_sel_hi:[1,0,0]
	v_mul_f32_e32 v23, 0x3fb8aa3b, v23
	v_exp_f32_e32 v22, v22
	v_pk_fma_f32 v[24:25], v[18:19], v[24:25], s[8:9] op_sel_hi:[1,1,0]
	v_exp_f32_e32 v23, v23
	v_pk_fma_f32 v[24:25], v[18:19], v[24:25], s[0:1] op_sel_hi:[1,1,0]
	s_nop 0
	v_pk_fma_f32 v[24:25], v[18:19], v[24:25], s[4:5] op_sel_hi:[1,1,0]
	s_nop 0
	v_pk_mul_f32 v[18:19], v[18:19], v[24:25]
	s_nop 0
	v_pk_fma_f32 v[18:19], v[22:23], v[18:19], 1.0 op_sel_hi:[1,1,0] neg_lo:[1,0,0] neg_hi:[1,0,0]
	s_nop 0
	v_bfi_b32 v11, s3, v19, v11
	v_bfi_b32 v10, s3, v18, v10
	v_pk_add_f32 v[10:11], v[10:11], 1.0 op_sel_hi:[1,0]
	s_nop 0
	v_pk_mul_f32 v[6:7], v[6:7], v[10:11]
	v_pk_fma_f32 v[10:11], v[40:41], v[68:69], v[20:21] op_sel_hi:[0,1,1] neg_lo:[1,0,0] neg_hi:[1,0,0]
	v_pk_fma_f32 v[10:11], v[40:41], v[10:11], v[70:71] op_sel:[1,0,0]
	v_cvt_pk_f16_f32 v126, v6, v7
	v_pk_add_f32 v[8:9], v[8:9], v[10:11]
	s_nop 0
	v_pk_mul_f32 v[10:11], v[8:9], s[6:7] op_sel_hi:[1,0]
	v_pk_mul_f32 v[8:9], v[8:9], 0.5 op_sel_hi:[1,0]
	v_fma_f32 v7, |v10|, s1, 1.0
	v_fma_f32 v19, |v11|, s1, 1.0
	v_rcp_f32_e32 v18, v7
	v_rcp_f32_e32 v19, v19
	v_mul_f32_e64 v7, |v10|, -|v10|
	v_mul_f32_e32 v7, 0x3fb8aa3b, v7
	v_exp_f32_e32 v20, v7
	v_mul_f32_e64 v7, |v11|, -|v11|
	v_pk_fma_f32 v[22:23], v[18:19], s[2:3], v[0:1] op_sel_hi:[1,0,0]
	v_mul_f32_e32 v7, 0x3fb8aa3b, v7
	v_pk_fma_f32 v[22:23], v[18:19], v[22:23], s[8:9] op_sel_hi:[1,1,0]
	v_exp_f32_e32 v21, v7
	v_pk_fma_f32 v[22:23], v[18:19], v[22:23], s[0:1] op_sel_hi:[1,1,0]
	s_nop 0
	v_pk_fma_f32 v[22:23], v[18:19], v[22:23], s[4:5] op_sel_hi:[1,1,0]
	s_nop 0
	v_pk_mul_f32 v[18:19], v[18:19], v[22:23]
	s_nop 0
	v_pk_fma_f32 v[18:19], v[20:21], v[18:19], 1.0 op_sel_hi:[1,1,0] neg_lo:[1,0,0] neg_hi:[1,0,0]
	s_nop 0
	v_bfi_b32 v11, s3, v19, v11
	v_bfi_b32 v10, s3, v18, v10
	v_pk_add_f32 v[10:11], v[10:11], 1.0 op_sel_hi:[1,0]
	s_nop 0
	v_pk_mul_f32 v[8:9], v[8:9], v[10:11]
	s_nop 0
	v_cvt_pk_f16_f32 v127, v8, v9
	v_lshl_add_u64 v[138:139], v[12:13], 0, v[118:119]
	s_nop 1
	v_permlane16_swap_b32 v124, v126
	v_permlane16_swap_b32 v125, v127
	global_store_dwordx4 v[138:139], v[124:127], off sc1
	v_pk_fma_f32 v[6:7], v[40:41], v[62:63], v[14:15] op_sel_hi:[0,1,1] neg_lo:[1,0,0] neg_hi:[1,0,0]
	v_pk_fma_f32 v[6:7], v[40:41], v[6:7], v[64:65] op_sel:[1,0,0]
	s_nop 0
	v_pk_add_f32 v[2:3], v[2:3], v[6:7]
	s_nop 0
	v_pk_mul_f32 v[6:7], v[2:3], s[6:7] op_sel_hi:[1,0]
	v_pk_mul_f32 v[2:3], v[2:3], 0.5 op_sel_hi:[1,0]
	v_fma_f32 v8, |v6|, s1, 1.0
	v_fma_f32 v9, |v7|, s1, 1.0
	v_rcp_f32_e32 v8, v8
	v_rcp_f32_e32 v9, v9
	v_mul_f32_e64 v10, |v6|, -|v6|
	v_mul_f32_e64 v11, |v7|, -|v7|
	v_mul_f32_e32 v10, 0x3fb8aa3b, v10
	v_pk_fma_f32 v[14:15], v[8:9], s[2:3], v[0:1] op_sel_hi:[1,0,0]
	v_mul_f32_e32 v11, 0x3fb8aa3b, v11
	v_exp_f32_e32 v10, v10
	v_pk_fma_f32 v[14:15], v[8:9], v[14:15], s[8:9] op_sel_hi:[1,1,0]
	v_exp_f32_e32 v11, v11
	v_pk_fma_f32 v[14:15], v[8:9], v[14:15], s[0:1] op_sel_hi:[1,1,0]
	s_nop 0
	v_pk_fma_f32 v[14:15], v[8:9], v[14:15], s[4:5] op_sel_hi:[1,1,0]
	s_nop 0
	v_pk_mul_f32 v[8:9], v[8:9], v[14:15]
	s_nop 0
	v_pk_fma_f32 v[8:9], v[10:11], v[8:9], 1.0 op_sel_hi:[1,1,0] neg_lo:[1,0,0] neg_hi:[1,0,0]
	s_nop 0
	v_bfi_b32 v7, s3, v9, v7
	v_bfi_b32 v6, s3, v8, v6
	v_pk_add_f32 v[6:7], v[6:7], 1.0 op_sel_hi:[1,0]
	s_nop 0
	v_pk_mul_f32 v[2:3], v[2:3], v[6:7]
	v_pk_fma_f32 v[6:7], v[40:41], v[58:59], v[16:17] op_sel_hi:[0,1,1] neg_lo:[1,0,0] neg_hi:[1,0,0]
	v_pk_fma_f32 v[6:7], v[40:41], v[6:7], v[66:67] op_sel:[1,0,0]
	v_cvt_pk_f16_f32 v134, v2, v3
	v_pk_add_f32 v[4:5], v[4:5], v[6:7]
	s_nop 0
	v_pk_mul_f32 v[6:7], v[4:5], s[6:7] op_sel_hi:[1,0]
	v_pk_mul_f32 v[4:5], v[4:5], 0.5 op_sel_hi:[1,0]
	v_fma_f32 v3, |v6|, s1, 1.0
	v_fma_f32 v9, |v7|, s1, 1.0
	v_rcp_f32_e32 v8, v3
	v_rcp_f32_e32 v9, v9
	v_mul_f32_e64 v3, |v6|, -|v6|
	v_mul_f32_e32 v3, 0x3fb8aa3b, v3
	v_exp_f32_e32 v10, v3
	v_mul_f32_e64 v3, |v7|, -|v7|
	v_pk_fma_f32 v[0:1], v[8:9], s[2:3], v[0:1] op_sel_hi:[1,0,0]
	v_mul_f32_e32 v3, 0x3fb8aa3b, v3
	v_pk_fma_f32 v[0:1], v[8:9], v[0:1], s[8:9] op_sel_hi:[1,1,0]
	v_exp_f32_e32 v11, v3
	v_pk_fma_f32 v[0:1], v[8:9], v[0:1], s[0:1] op_sel_hi:[1,1,0]
	s_nop 0
	v_pk_fma_f32 v[0:1], v[8:9], v[0:1], s[4:5] op_sel_hi:[1,1,0]
	s_nop 0
	v_pk_mul_f32 v[0:1], v[8:9], v[0:1]
	s_nop 0
	v_pk_fma_f32 v[0:1], v[10:11], v[0:1], 1.0 op_sel_hi:[1,1,0] neg_lo:[1,0,0] neg_hi:[1,0,0]
	s_nop 0
	v_bfi_b32 v1, s3, v1, v7
	v_bfi_b32 v0, s3, v0, v6
	v_pk_add_f32 v[0:1], v[0:1], 1.0 op_sel_hi:[1,0]
	s_nop 0
	v_pk_mul_f32 v[0:1], v[4:5], v[0:1]
	s_nop 0
	v_cvt_pk_f16_f32 v135, v0, v1
	v_lshl_add_u64 v[138:139], v[12:13], 0, v[136:137]
	s_nop 1
	v_permlane16_swap_b32 v132, v134
	v_permlane16_swap_b32 v133, v135
	global_store_dwordx4 v[138:139], v[132:135], off sc1
	s_endpgm
	.p2align	8

.LBB9_9:
	s_lshr_b32 s9, s3, 29
	s_add_i32 s9, s3, s9
	s_and_b32 s9, s9, 0xffff8
	s_sub_i32 s3, s3, s9
	s_mulk_i32 s3, 0x5000
	s_add_i32 s3, s3, 0
	v_add_u32_e32 v51, s3, v50
	v_lshlrev_b32_e32 v60, 1, v53
	v_add_u32_e32 v53, s3, v0
	v_add_u32_e32 v52, v51, v60
	v_add_u32_e32 v55, v53, v60
	s_waitcnt vmcnt(25)
	s_barrier
	ds_read_b128 v[56:59], v52 offset:8192
	ds_read_b128 v[74:77], v55
	ds_read_b128 v[78:81], v52 offset:10240
	ds_read_b128 v[82:85], v55 offset:2048
	ds_read_b128 v[86:89], v52 offset:12288
	v_lshlrev_b32_e32 v73, 1, v54
	v_add_u32_e32 v51, v51, v73
	s_waitcnt lgkmcnt(3)
	v_mfma_f32_16x16x32_f16 a[0:3], v[56:59], v[74:77], a[0:3]
	v_add_u32_e32 v61, v53, v73
	s_add_i32 s3, s24, -5
	s_lshr_b32 s9, s3, 29
	s_waitcnt lgkmcnt(2)
	v_mfma_f32_16x16x32_f16 a[4:7], v[78:81], v[74:77], a[4:7]
	s_add_i32 s9, s3, s9
	s_and_b32 s9, s9, 0xffff8
	s_sub_i32 s3, s3, s9
	s_waitcnt lgkmcnt(1)
	v_mfma_f32_16x16x32_f16 a[12:15], v[56:59], v[82:85], a[12:15]
	ds_read_b128 v[56:59], v51 offset:8192
	s_mulk_i32 s3, 0x5000
	s_add_i32 s3, s3, 0
	v_mfma_f32_16x16x32_f16 a[16:19], v[78:81], v[82:85], a[16:19]
	ds_read_b128 v[78:81], v51 offset:12288
	ds_read_b128 v[52:55], v61
	v_lshlrev_b32_e32 v72, 2, v71
	s_waitcnt lgkmcnt(3)
	v_mfma_f32_16x16x32_f16 a[8:11], v[86:89], v[74:77], a[8:11]
	ds_read_b128 v[74:77], v51 offset:10240
	v_add_u32_e32 v51, s3, v50
	s_load_dwordx2 s[0:1], s[0:1], 0x50
	s_waitcnt lgkmcnt(0)
	v_mfma_f32_16x16x32_f16 a[0:3], v[56:59], v[52:55], a[0:3]
	v_mfma_f32_16x16x32_f16 a[4:7], v[74:77], v[52:55], a[4:7]
	v_mfma_f32_16x16x32_f16 a[8:11], v[78:81], v[52:55], a[8:11]
	ds_read_b128 v[52:55], v61 offset:2048
	v_add_u32_e32 v61, v51, v60
	s_waitcnt vmcnt(20)
	v_mfma_f32_16x16x32_f16 a[20:23], v[86:89], v[82:85], a[20:23]
	s_barrier
	v_add_u32_e32 v86, s3, v0
	v_add_u32_e32 v51, v51, v73
	s_waitcnt lgkmcnt(0)
	v_mfma_f32_16x16x32_f16 a[12:15], v[56:59], v[52:55], a[12:15]
	s_add_i32 s3, s24, -4
	s_lshr_b32 s9, s3, 29
	s_add_i32 s9, s3, s9
	v_mfma_f32_16x16x32_f16 a[16:19], v[74:77], v[52:55], a[16:19]
	s_and_b32 s9, s9, 0xffff8
	s_sub_i32 s3, s3, s9
	s_mulk_i32 s3, 0x5000
	v_mfma_f32_16x16x32_f16 a[20:23], v[78:81], v[52:55], a[20:23]
	ds_read_b128 v[52:55], v61 offset:8192
	v_add_u32_e32 v78, v86, v60
	ds_read_b128 v[56:59], v61 offset:10240
	ds_read_b128 v[74:77], v78
	ds_read_b128 v[78:81], v78 offset:2048
	ds_read_b128 v[82:85], v61 offset:12288
	v_add_u32_e32 v61, v86, v73
	s_waitcnt lgkmcnt(2)
	v_mfma_f32_16x16x32_f16 a[0:3], v[52:55], v[74:77], a[0:3]
	ds_read_b128 v[86:89], v61
	s_add_i32 s3, s3, 0
	s_waitcnt lgkmcnt(2)
	v_mfma_f32_16x16x32_f16 a[12:15], v[52:55], v[78:81], a[12:15]
	ds_read_b128 v[52:55], v51 offset:8192
	v_mfma_f32_16x16x32_f16 a[4:7], v[56:59], v[74:77], a[4:7]
	s_waitcnt lgkmcnt(2)
	v_mfma_f32_16x16x32_f16 a[8:11], v[82:85], v[74:77], a[8:11]
	v_mfma_f32_16x16x32_f16 a[16:19], v[56:59], v[78:81], a[16:19]
	ds_read_b128 v[56:59], v51 offset:10240
	ds_read_b128 v[74:77], v51 offset:12288
	v_add_u32_e32 v51, s3, v0
	v_mfma_f32_16x16x32_f16 a[20:23], v[82:85], v[78:81], a[20:23]
	ds_read_b128 v[78:81], v61 offset:2048
	v_add_u32_e32 v61, s3, v50
	v_add_u32_e32 v82, v61, v60
	s_waitcnt lgkmcnt(3)
	v_mfma_f32_16x16x32_f16 a[0:3], v[52:55], v[86:89], a[0:3]
	s_waitcnt vmcnt(15)
	s_barrier
	v_add_u32_e32 v83, v51, v60
	s_waitcnt lgkmcnt(0)
	v_mfma_f32_16x16x32_f16 a[12:15], v[52:55], v[78:81], a[12:15]
	ds_read_b128 v[52:55], v82 offset:8192
	v_add_u32_e32 v51, v51, v73
	v_add_u32_e32 v61, v61, v73
	v_mfma_f32_16x16x32_f16 a[4:7], v[56:59], v[86:89], a[4:7]
	s_add_i32 s3, s24, -3
	s_lshr_b32 s9, s3, 29
	s_add_i32 s9, s3, s9
	v_mfma_f32_16x16x32_f16 a[8:11], v[74:77], v[86:89], a[8:11]
	s_and_b32 s9, s9, 0xffff8
	s_sub_i32 s3, s3, s9
	s_mulk_i32 s3, 0x5000
	v_mfma_f32_16x16x32_f16 a[16:19], v[56:59], v[78:81], a[16:19]
	s_add_i32 s3, s3, 0
	v_mfma_f32_16x16x32_f16 a[20:23], v[74:77], v[78:81], a[20:23]
	ds_read_b128 v[56:59], v82 offset:10240
	ds_read_b128 v[74:77], v83
	ds_read_b128 v[78:81], v83 offset:2048
	ds_read_b128 v[82:85], v82 offset:12288
	ds_read_b128 v[86:89], v51
	s_waitcnt lgkmcnt(3)
	v_mfma_f32_16x16x32_f16 a[0:3], v[52:55], v[74:77], a[0:3]
	s_waitcnt lgkmcnt(2)
	v_mfma_f32_16x16x32_f16 a[12:15], v[52:55], v[78:81], a[12:15]
	ds_read_b128 v[52:55], v61 offset:8192
	v_mfma_f32_16x16x32_f16 a[4:7], v[56:59], v[74:77], a[4:7]
	s_waitcnt lgkmcnt(2)
	v_mfma_f32_16x16x32_f16 a[8:11], v[82:85], v[74:77], a[8:11]
	v_mfma_f32_16x16x32_f16 a[16:19], v[56:59], v[78:81], a[16:19]
	v_mfma_f32_16x16x32_f16 a[20:23], v[82:85], v[78:81], a[20:23]
	ds_read_b128 v[56:59], v61 offset:10240
	ds_read_b128 v[74:77], v51 offset:2048
	ds_read_b128 v[78:81], v61 offset:12288
	v_add_u32_e32 v61, s3, v50
	v_add_u32_e32 v82, v61, v60
	s_waitcnt lgkmcnt(3)
	v_mfma_f32_16x16x32_f16 a[0:3], v[52:55], v[86:89], a[0:3]
	s_waitcnt vmcnt(10)
	s_barrier
	v_add_u32_e32 v51, s3, v0
	s_waitcnt lgkmcnt(1)
	v_mfma_f32_16x16x32_f16 a[12:15], v[52:55], v[74:77], a[12:15]
	ds_read_b128 v[52:55], v82 offset:8192
	v_add_u32_e32 v83, v51, v60
	v_add_u32_e32 v51, v51, v73
	v_mfma_f32_16x16x32_f16 a[4:7], v[56:59], v[86:89], a[4:7]
	v_add_u32_e32 v61, v61, v73
	s_add_i32 s3, s24, -2
	s_lshr_b32 s9, s3, 29
	s_waitcnt lgkmcnt(1)
	v_mfma_f32_16x16x32_f16 a[8:11], v[78:81], v[86:89], a[8:11]
	s_add_i32 s9, s3, s9
	s_and_b32 s9, s9, 0xffff8
	s_sub_i32 s3, s3, s9
	v_mfma_f32_16x16x32_f16 a[16:19], v[56:59], v[74:77], a[16:19]
	ds_read_b128 v[56:59], v82 offset:10240
	s_mulk_i32 s3, 0x5000
	s_add_i32 s3, s3, 0
	v_mfma_f32_16x16x32_f16 a[20:23], v[78:81], v[74:77], a[20:23]
	ds_read_b128 v[74:77], v83
	ds_read_b128 v[78:81], v83 offset:2048
	ds_read_b128 v[82:85], v82 offset:12288
	ds_read_b128 v[86:89], v51
	s_waitcnt lgkmcnt(3)
	v_mfma_f32_16x16x32_f16 a[0:3], v[52:55], v[74:77], a[0:3]
	s_waitcnt lgkmcnt(2)
	v_mfma_f32_16x16x32_f16 a[12:15], v[52:55], v[78:81], a[12:15]
	ds_read_b128 v[52:55], v61 offset:8192
	v_mfma_f32_16x16x32_f16 a[4:7], v[56:59], v[74:77], a[4:7]
	s_waitcnt lgkmcnt(2)
	v_mfma_f32_16x16x32_f16 a[8:11], v[82:85], v[74:77], a[8:11]
	v_mfma_f32_16x16x32_f16 a[16:19], v[56:59], v[78:81], a[16:19]
	v_mfma_f32_16x16x32_f16 a[20:23], v[82:85], v[78:81], a[20:23]
	ds_read_b128 v[56:59], v61 offset:10240
	ds_read_b128 v[74:77], v51 offset:2048
	ds_read_b128 v[78:81], v61 offset:12288
	v_add_u32_e32 v61, s3, v50
	v_add_u32_e32 v82, v61, v60
	s_waitcnt lgkmcnt(3)
	v_mfma_f32_16x16x32_f16 a[0:3], v[52:55], v[86:89], a[0:3]
	s_waitcnt vmcnt(5)
	s_barrier
	v_add_u32_e32 v51, s3, v0
	s_waitcnt lgkmcnt(1)
	v_mfma_f32_16x16x32_f16 a[12:15], v[52:55], v[74:77], a[12:15]
	ds_read_b128 v[52:55], v82 offset:8192
	v_add_u32_e32 v83, v51, v60
	v_add_u32_e32 v51, v51, v73
	v_mfma_f32_16x16x32_f16 a[4:7], v[56:59], v[86:89], a[4:7]
	v_add_u32_e32 v61, v61, v73
	s_add_i32 s3, s24, -1
	s_lshr_b32 s9, s3, 29
	s_waitcnt lgkmcnt(1)
	v_mfma_f32_16x16x32_f16 a[8:11], v[78:81], v[86:89], a[8:11]
	s_add_i32 s9, s3, s9
	s_and_b32 s9, s9, 0xffff8
	s_sub_i32 s3, s3, s9
	v_mfma_f32_16x16x32_f16 a[16:19], v[56:59], v[74:77], a[16:19]
	ds_read_b128 v[56:59], v82 offset:10240
	s_mulk_i32 s3, 0x5000
	s_add_i32 s3, s3, 0
	v_mfma_f32_16x16x32_f16 a[20:23], v[78:81], v[74:77], a[20:23]
	ds_read_b128 v[74:77], v83
	ds_read_b128 v[78:81], v83 offset:2048
	ds_read_b128 v[82:85], v82 offset:12288
	ds_read_b128 v[86:89], v51
	s_waitcnt lgkmcnt(3)
	v_mfma_f32_16x16x32_f16 a[0:3], v[52:55], v[74:77], a[0:3]
	v_add_u32_e32 v0, s3, v0
	s_waitcnt lgkmcnt(2)
	v_mfma_f32_16x16x32_f16 a[12:15], v[52:55], v[78:81], a[12:15]
	ds_read_b128 v[52:55], v61 offset:8192
	v_mfma_f32_16x16x32_f16 a[4:7], v[56:59], v[74:77], a[4:7]
	s_waitcnt lgkmcnt(2)
	v_mfma_f32_16x16x32_f16 a[8:11], v[82:85], v[74:77], a[8:11]
	v_mfma_f32_16x16x32_f16 a[16:19], v[56:59], v[78:81], a[16:19]
	v_mfma_f32_16x16x32_f16 a[20:23], v[82:85], v[78:81], a[20:23]
	ds_read_b128 v[56:59], v61 offset:10240
	ds_read_b128 v[74:77], v51 offset:2048
	ds_read_b128 v[78:81], v61 offset:12288
	s_waitcnt vmcnt(0)
	s_barrier
	s_waitcnt lgkmcnt(3)
	v_mfma_f32_16x16x32_f16 a[0:3], v[52:55], v[86:89], a[0:3]
	v_add_u32_e32 v83, v0, v60
	v_add_u32_e32 v0, v0, v73
	s_waitcnt lgkmcnt(2)
	v_mfma_f32_16x16x32_f16 a[4:7], v[56:59], v[86:89], a[4:7]
	s_waitcnt lgkmcnt(0)
	v_mfma_f32_16x16x32_f16 a[8:11], v[78:81], v[86:89], a[8:11]
	v_add_u32_e32 v86, s3, v50
	v_add_u32_e32 v82, v86, v60
	v_add_u32_e32 v73, v86, v73
	v_mfma_f32_16x16x32_f16 a[12:15], v[52:55], v[74:77], a[12:15]
	ds_read_b128 v[50:53], v82 offset:8192
	v_mfma_f32_16x16x32_f16 a[16:19], v[56:59], v[74:77], a[16:19]
	ds_read_b128 v[54:57], v82 offset:10240
	v_mfma_f32_16x16x32_f16 a[20:23], v[78:81], v[74:77], a[20:23]
	ds_read_b128 v[58:61], v83
	ds_read_b128 v[74:77], v83 offset:2048
	ds_read_b128 v[78:81], v82 offset:12288
	ds_read_b128 v[82:85], v0
	s_waitcnt lgkmcnt(3)
	v_mfma_f32_16x16x32_f16 a[0:3], v[50:53], v[58:61], a[0:3]
	s_waitcnt lgkmcnt(2)
	v_mfma_f32_16x16x32_f16 a[12:15], v[50:53], v[74:77], a[12:15]
	ds_read_b128 v[50:53], v73 offset:8192
	v_mfma_f32_16x16x32_f16 a[4:7], v[54:57], v[58:61], a[4:7]
	s_waitcnt lgkmcnt(2)
	v_mfma_f32_16x16x32_f16 a[8:11], v[78:81], v[58:61], a[8:11]
	v_mfma_f32_16x16x32_f16 a[16:19], v[54:57], v[74:77], a[16:19]
	v_mfma_f32_16x16x32_f16 a[20:23], v[78:81], v[74:77], a[20:23]
	ds_read_b128 v[54:57], v73 offset:10240
	ds_read_b128 v[58:61], v0 offset:2048
	ds_read_b128 v[74:77], v73 offset:12288
	v_or_b32_e32 v0, v72, v70
	v_add_u32_e32 v70, s2, v0
	s_waitcnt lgkmcnt(3)
	v_mfma_f32_16x16x32_f16 a[0:3], v[50:53], v[82:85], a[0:3]
	v_mbcnt_lo_u32_b32 v0, -1, 0
	v_mbcnt_hi_u32_b32 v0, -1, v0
	v_and_b32_e32 v72, 64, v0
	s_waitcnt vmcnt(6)
	v_mov_b32_e32 v79, v27
	s_waitcnt lgkmcnt(2)
	v_mfma_f32_16x16x32_f16 a[4:7], v[54:57], v[82:85], a[4:7]
	v_xor_b32_e32 v27, 16, v0
	v_add_u32_e32 v72, 64, v72
	v_cmp_lt_i32_e32 vcc, v27, v72
	v_accvgpr_read_b32 v80, a3
	v_accvgpr_read_b32 v86, a2
	v_accvgpr_read_b32 v89, a1
	v_accvgpr_read_b32 v88, a0
	s_waitcnt lgkmcnt(1)
	v_mfma_f32_16x16x32_f16 a[0:3], v[50:53], v[58:61], a[12:15]
	v_cndmask_b32_e32 v27, v0, v27, vcc
	v_lshlrev_b32_e32 v73, 2, v27
	v_xor_b32_e32 v27, 32, v0
	s_waitcnt lgkmcnt(0)
	v_mfma_f32_16x16x32_f16 a[8:11], v[74:77], v[82:85], a[8:11]
	v_accvgpr_read_b32 v82, a7
	v_accvgpr_read_b32 v84, a6
	v_accvgpr_read_b32 v91, a5
	v_accvgpr_read_b32 v90, a4
	v_mfma_f32_16x16x32_f16 a[4:7], v[54:57], v[58:61], a[16:19]
	v_accvgpr_read_b32 v57, a3
	v_cmp_lt_i32_e32 vcc, v27, v72
	v_accvgpr_read_b32 v56, a2
	v_accvgpr_read_b32 v55, a1
	v_accvgpr_read_b32 v54, a0
	v_mfma_f32_16x16x32_f16 a[0:3], v[74:77], v[58:61], a[20:23]
	v_cndmask_b32_e32 v0, v0, v27, vcc
	v_cmp_eq_u32_e32 vcc, 0, v71
	v_lshl_add_u64 v[74:75], v[68:69], 2, s[4:5]
	v_ashrrev_i32_e32 v71, 31, v70
	v_lshl_add_u64 v[94:95], v[70:71], 2, v[74:75]
	v_accvgpr_read_b32 v75, a9
	v_accvgpr_read_b32 v74, a8
	v_accvgpr_read_b32 v93, a11
	v_accvgpr_read_b32 v92, a10
	s_waitcnt vmcnt(2)
	v_pk_add_f32 v[74:75], v[30:31], v[74:75]
	v_lshl_add_u64 v[68:69], v[68:69], 1, s[6:7]
	v_pk_add_f32 v[74:75], v[46:47], v[74:75]
	v_pk_add_f32 v[46:47], v[32:33], v[92:93]
	v_fma_mixlo_f16 v27, v22, v74, 0
	v_pk_add_f32 v[76:77], v[48:49], v[46:47]
	v_pk_mov_b32 v[46:47], v[22:23], v[24:25] op_sel:[1,0]
	v_pk_mov_b32 v[48:49], v[74:75], v[76:77] op_sel:[1,0]
	v_lshl_add_u64 v[68:69], v[70:71], 1, v[68:69]
	v_pk_mul_f32 v[46:47], v[46:47], v[48:49]
	v_mov_b32_e32 v78, v26
	v_cvt_pk_f16_f32 v47, v46, v47
	v_pack_b32_f16 v46, v27, v47
	v_fma_mixlo_f16 v27, v25, v77, 0
	v_alignbit_b32 v47, v27, v47, 16
	global_store_dwordx2 v[68:69], v[46:47], off offset:64 sc1
	v_mov_b32_e32 v27, v18
	v_mov_b32_e32 v46, v88
	v_mov_b32_e32 v47, v90
	v_pk_add_f32 v[96:97], v[26:27], v[46:47]
	v_pk_mov_b32 v[46:47], v[78:79], v[18:19] op_sel:[1,0]
	v_pk_mov_b32 v[78:79], v[88:89], v[90:91] op_sel:[1,0]
	v_mov_b32_e32 v88, v18
	v_mov_b32_e32 v89, v42
	v_mov_b32_e32 v98, v90
	v_mov_b32_e32 v99, v96
	v_pk_add_f32 v[78:79], v[46:47], v[78:79]
	v_pk_add_f32 v[88:89], v[88:89], v[98:99]
	v_mov_b32_e32 v98, v42
	v_mov_b32_e32 v99, v38
	v_pk_add_f32 v[96:97], v[98:99], v[96:97]
	v_pk_mov_b32 v[98:99], v[42:43], v[38:39] op_sel:[1,0]
	v_mov_b32_e32 v42, v19
	v_mov_b32_e32 v100, v91
	v_mov_b32_e32 v101, v78
	v_pk_add_f32 v[100:101], v[42:43], v[100:101]
	v_mov_b32_e32 v42, v28
	v_mov_b32_e32 v43, v19
	v_mov_b32_e32 v87, v91
	v_pk_add_f32 v[98:99], v[98:99], v[78:79]
	v_pk_add_f32 v[78:79], v[42:43], v[86:87]
	v_mov_b32_e32 v28, v29
	v_mov_b32_e32 v29, v19
	v_mov_b32_e32 v81, v91
	v_pk_add_f32 v[80:81], v[28:29], v[80:81]
	v_mov_b32_e32 v86, v20
	v_mov_b32_e32 v87, v44
	v_mov_b32_e32 v85, v78
	v_pk_add_f32 v[84:85], v[86:87], v[84:85]
	v_mov_b32_e32 v86, v44
	v_mov_b32_e32 v44, v21
	v_mov_b32_e32 v83, v80
	v_mov_b32_e32 v87, v39
	v_pk_add_f32 v[82:83], v[44:45], v[82:83]
	v_mov_b32_e32 v44, v45
	v_mov_b32_e32 v45, v39
	v_pk_add_f32 v[86:87], v[86:87], v[78:79]
	v_pk_add_f32 v[44:45], v[44:45], v[80:81]
	v_mov_b32_e32 v78, v89
	v_mov_b32_e32 v79, v101
	v_mov_b32_e32 v80, v85
	v_mov_b32_e32 v81, v83
	global_store_dwordx4 v[94:95], v[78:81], off sc1
	v_fma_mixlo_f16 v90, v6, v89, 0
	global_store_dwordx4 v[94:95], v[74:77], off offset:128 sc1
	v_pk_mov_b32 v[78:79], v[6:7], v[8:9] op_sel:[1,0]
	v_mov_b32_e32 v80, v101
	v_mov_b32_e32 v81, v85
	v_pk_mul_f32 v[78:79], v[78:79], v[80:81]
	v_fma_mixlo_f16 v80, v9, v83, 0
	v_cvt_pk_f16_f32 v79, v78, v79
	v_pack_b32_f16 v78, v90, v79
	v_alignbit_b32 v79, v80, v79, 16
	global_store_dwordx2 v[68:69], v[78:79], off sc1
	v_mov_b32_e32 v78, v38
	v_mov_b32_e32 v79, v89
	v_pk_add_f32 v[78:79], v[78:79], v[88:89]
	v_pk_mul_f32 v[80:81], v[88:89], v[88:89]
	v_mov_b32_e32 v38, v39
	v_mov_b32_e32 v39, v101
	v_mov_b32_e32 v79, v81
	v_pk_add_f32 v[80:81], v[38:39], v[100:101]
	v_pk_mul_f32 v[38:39], v[100:101], v[100:101]
	v_pk_mul_f32 v[90:91], v[96:97], v[98:99]
	v_mov_b32_e32 v81, v39
	v_mov_b32_e32 v38, v40
	v_mov_b32_e32 v39, v85
	v_pk_add_f32 v[88:89], v[38:39], v[84:85]
	v_pk_mul_f32 v[38:39], v[84:85], v[84:85]
	v_mov_b32_e32 v40, v88
	v_mov_b32_e32 v89, v39
	v_mov_b32_e32 v38, v41
	v_mov_b32_e32 v39, v83
	v_pk_add_f32 v[84:85], v[38:39], v[82:83]
	v_pk_mul_f32 v[38:39], v[82:83], v[82:83]
	v_mov_b32_e32 v41, v84
	v_mov_b32_e32 v85, v39
	v_mov_b32_e32 v38, v78
	v_mov_b32_e32 v39, v80
	global_store_dwordx4 v[94:95], v[38:41], off offset:64 sc1
	v_fma_mixlo_f16 v94, v2, v78, 0
	v_mov_b32_e32 v82, v88
	v_pk_add_f32 v[38:39], v[78:79], v[80:81]
	v_pk_add_f32 v[78:79], v[88:89], v[84:85]
	v_mov_b32_e32 v83, v84
	v_pk_add_f32 v[78:79], v[38:39], v[78:79]
	v_pk_add_f32 v[38:39], v[96:97], v[98:99]
	v_pk_mul_f32 v[48:49], v[74:75], v[74:75]
	v_mov_b32_e32 v39, v91
	v_pk_add_f32 v[90:91], v[86:87], v[44:45]
	v_pk_mul_f32 v[44:45], v[86:87], v[44:45]
	v_pk_mul_f32 v[92:93], v[76:77], v[76:77]
	v_mov_b32_e32 v91, v45
	v_pk_add_f32 v[44:45], v[38:39], v[90:91]
	v_mul_f32_e32 v38, v88, v88
	v_pk_fma_f32 v[38:39], v[82:83], v[82:83], v[38:39] op_sel_hi:[1,1,0]
	v_pk_mov_b32 v[40:41], v[2:3], v[4:5] op_sel:[1,0]
	v_mov_b32_e32 v38, 0
	v_pk_add_f32 v[44:45], v[44:45], v[38:39]
	v_mov_b32_e32 v81, v88
	v_pk_add_f32 v[44:45], v[78:79], v[44:45]
	v_mov_b32_e32 v78, v74
	v_mov_b32_e32 v79, v48
	v_mov_b32_e32 v48, v75
	v_mov_b32_e32 v74, v76
	v_mov_b32_e32 v75, v92
	v_mov_b32_e32 v92, v77
	v_pk_add_f32 v[48:49], v[78:79], v[48:49]
	v_pk_add_f32 v[74:75], v[74:75], v[92:93]
	v_pk_mul_f32 v[40:41], v[40:41], v[80:81]
	v_pk_add_f32 v[48:49], v[48:49], v[74:75]
	v_lshlrev_b32_e32 v72, 2, v0
	v_pk_add_f32 v[44:45], v[44:45], v[48:49]
	ds_bpermute_b32 v48, v73, v44
	ds_bpermute_b32 v49, v73, v45
	v_cvt_pk_f16_f32 v39, v40, v41
	v_accvgpr_read_b32 v53, a7
	v_accvgpr_read_b32 v61, a3
	v_lshl_or_b32 v0, s11, 1, v1
	s_waitcnt lgkmcnt(0)
	v_pk_add_f32 v[40:41], v[44:45], v[48:49]
	ds_bpermute_b32 v44, v72, v40
	ds_bpermute_b32 v45, v72, v41
	v_fma_mixlo_f16 v49, v5, v84, 0
	v_accvgpr_read_b32 v52, a6
	v_accvgpr_read_b32 v51, a5
	v_accvgpr_read_b32 v50, a4
	v_accvgpr_read_b32 v60, a2
	v_accvgpr_read_b32 v59, a1
	v_accvgpr_read_b32 v58, a0
	v_mad_i64_i32 v[0:1], s[2:3], v0, s8, 0
	v_pack_b32_f16 v48, v94, v39
	v_alignbit_b32 v49, v49, v39, 16
	global_store_dwordx2 v[68:69], v[48:49], off offset:32 sc1
	s_and_saveexec_b64 s[2:3], vcc
	s_cbranch_execz .LBB9_11
	v_lshl_add_u64 v[48:49], v[0:1], 0, v[64:65]
	v_lshl_add_u64 v[48:49], v[48:49], 3, s[0:1]
	s_waitcnt lgkmcnt(0)
	v_pk_add_f32 v[40:41], v[40:41], v[44:45]
	global_store_dwordx2 v[48:49], v[40:41], off sc1
.LBB9_11:
	s_or_b64 exec, exec, s[2:3]
	v_pk_add_f32 v[30:31], v[30:31], v[58:59]
	v_pk_add_f32 v[32:33], v[32:33], v[60:61]
	s_waitcnt vmcnt(6)
	v_pk_add_f32 v[30:31], v[34:35], v[30:31]
	v_mov_b32_e32 v34, v54
	v_mov_b32_e32 v35, v50
	v_pk_add_f32 v[26:27], v[26:27], v[34:35]
	v_pk_mov_b32 v[34:35], v[54:55], v[50:51] op_sel:[1,0]
	v_pk_add_f32 v[32:33], v[36:37], v[32:33]
	v_pk_add_f32 v[34:35], v[46:47], v[34:35]
	v_mov_b32_e32 v36, v18
	v_mov_b32_e32 v37, v14
	v_mov_b32_e32 v46, v50
	v_mov_b32_e32 v47, v26
	v_pk_add_f32 v[36:37], v[36:37], v[46:47]
	v_mov_b32_e32 v46, v14
	v_mov_b32_e32 v47, v10
	v_pk_add_f32 v[26:27], v[46:47], v[26:27]
	v_pk_mov_b32 v[46:47], v[14:15], v[10:11] op_sel:[1,0]
	v_mov_b32_e32 v14, v19
	v_mov_b32_e32 v18, v51
	v_mov_b32_e32 v19, v34
	v_mov_b32_e32 v50, v56
	v_pk_add_f32 v[18:19], v[14:15], v[18:19]
	v_pk_add_f32 v[14:15], v[42:43], v[50:51]
	v_mov_b32_e32 v50, v57
	v_mov_b32_e32 v42, v20
	v_mov_b32_e32 v43, v16
	v_mov_b32_e32 v48, v52
	v_mov_b32_e32 v49, v14
	v_pk_add_f32 v[28:29], v[28:29], v[50:51]
	v_pk_add_f32 v[42:43], v[42:43], v[48:49]
	v_mov_b32_e32 v48, v16
	v_mov_b32_e32 v49, v11
	v_pk_add_f32 v[48:49], v[48:49], v[14:15]
	v_mov_b32_e32 v16, v21
	v_mov_b32_e32 v14, v53
	v_mov_b32_e32 v15, v28
	v_pk_add_f32 v[20:21], v[16:17], v[14:15]
	v_pk_add_f32 v[46:47], v[46:47], v[34:35]
	v_mov_b32_e32 v34, v37
	v_mov_b32_e32 v35, v19
	v_mov_b32_e32 v50, v43
	v_mov_b32_e32 v51, v21
	s_waitcnt lgkmcnt(0)
	v_lshl_add_u64 v[44:45], v[66:67], 1, s[6:7]
	v_pk_mul_f32 v[6:7], v[6:7], v[34:35]
	v_pk_mul_f32 v[8:9], v[8:9], v[50:51]
	v_lshl_add_u64 v[44:45], v[70:71], 1, v[44:45]
	v_cvt_pk_f16_f32 v6, v6, v7
	v_cvt_pk_f16_f32 v7, v8, v9
	global_store_dwordx2 v[44:45], v[6:7], off sc1
	v_mov_b32_e32 v6, v10
	v_mov_b32_e32 v7, v37
	v_pk_add_f32 v[8:9], v[6:7], v[36:37]
	v_pk_mul_f32 v[6:7], v[36:37], v[36:37]
	v_lshl_add_u64 v[40:41], v[66:67], 2, s[4:5]
	v_mov_b32_e32 v9, v7
	v_mov_b32_e32 v6, v11
	v_mov_b32_e32 v7, v19
	v_mov_b32_e32 v14, v17
	v_mov_b32_e32 v15, v11
	v_pk_add_f32 v[10:11], v[6:7], v[18:19]
	v_pk_mul_f32 v[6:7], v[18:19], v[18:19]
	v_lshl_add_u64 v[40:41], v[70:71], 2, v[40:41]
	v_pk_add_f32 v[28:29], v[14:15], v[28:29]
	v_mov_b32_e32 v14, v37
	v_mov_b32_e32 v15, v19
	v_mov_b32_e32 v16, v43
	v_mov_b32_e32 v17, v21
	v_mov_b32_e32 v11, v7
	v_mov_b32_e32 v6, v12
	v_mov_b32_e32 v7, v43
	global_store_dwordx4 v[40:41], v[14:17], off sc1
	v_pk_mul_f32 v[22:23], v[22:23], v[30:31]
	v_pk_mul_f32 v[24:25], v[24:25], v[32:33]
	v_pk_add_f32 v[14:15], v[6:7], v[42:43]
	v_pk_mul_f32 v[6:7], v[42:43], v[42:43]
	v_mov_b32_e32 v16, v8
	v_mov_b32_e32 v15, v7
	v_mov_b32_e32 v6, v13
	v_mov_b32_e32 v7, v21
	v_pk_add_f32 v[12:13], v[6:7], v[20:21]
	v_pk_mul_f32 v[6:7], v[20:21], v[20:21]
	v_mov_b32_e32 v17, v10
	v_mov_b32_e32 v13, v7
	v_mov_b32_e32 v6, v8
	v_mov_b32_e32 v7, v10
	v_pk_add_f32 v[8:9], v[8:9], v[10:11]
	v_pk_add_f32 v[10:11], v[14:15], v[12:13]
	v_pk_mul_f32 v[20:21], v[26:27], v[46:47]
	v_pk_add_f32 v[8:9], v[8:9], v[10:11]
	v_pk_add_f32 v[10:11], v[26:27], v[46:47]
	v_pk_mul_f32 v[26:27], v[48:49], v[28:29]
	v_mov_b32_e32 v11, v21
	v_pk_add_f32 v[20:21], v[48:49], v[28:29]
	v_mov_b32_e32 v18, v14
	v_mov_b32_e32 v21, v27
	v_mov_b32_e32 v19, v12
	v_pk_add_f32 v[10:11], v[10:11], v[20:21]
	v_mul_f32_e32 v20, v14, v14
	v_pk_fma_f32 v[20:21], v[18:19], v[18:19], v[20:21] op_sel_hi:[1,1,0]
	v_cvt_pk_f16_f32 v22, v22, v23
	v_cvt_pk_f16_f32 v23, v24, v25
	v_mov_b32_e32 v39, v21
	global_store_dwordx2 v[44:45], v[22:23], off offset:64 sc1
	v_pk_mul_f32 v[22:23], v[30:31], v[30:31]
	v_pk_mul_f32 v[24:25], v[32:33], v[32:33]
	v_pk_add_f32 v[10:11], v[10:11], v[38:39]
	v_mov_b32_e32 v20, v32
	v_pk_add_f32 v[8:9], v[8:9], v[10:11]
	v_mov_b32_e32 v10, v30
	v_mov_b32_e32 v11, v22
	v_mov_b32_e32 v22, v31
	v_mov_b32_e32 v21, v24
	v_mov_b32_e32 v24, v33
	v_pk_add_f32 v[10:11], v[10:11], v[22:23]
	v_pk_add_f32 v[20:21], v[20:21], v[24:25]
	v_pk_mul_f32 v[4:5], v[4:5], v[18:19]
	v_pk_add_f32 v[10:11], v[10:11], v[20:21]
	global_store_dwordx4 v[40:41], v[30:33], off offset:128 sc1
	v_pk_add_f32 v[10:11], v[8:9], v[10:11]
	ds_bpermute_b32 v20, v73, v10
	ds_bpermute_b32 v21, v73, v11
	v_mov_b32_e32 v8, v14
	v_mov_b32_e32 v9, v12
	global_store_dwordx4 v[40:41], v[6:9], off offset:64 sc1
	s_nop 1
	v_pk_mul_f32 v[8:9], v[2:3], v[16:17]
	s_waitcnt lgkmcnt(0)
	v_pk_add_f32 v[2:3], v[10:11], v[20:21]
	ds_bpermute_b32 v6, v72, v2
	ds_bpermute_b32 v7, v72, v3
	v_cvt_pk_f16_f32 v8, v8, v9
	v_cvt_pk_f16_f32 v9, v4, v5
	global_store_dwordx2 v[44:45], v[8:9], off offset:32 sc1
	s_and_saveexec_b64 s[2:3], vcc
	s_cbranch_execz .LBB9_13
	v_lshl_add_u64 v[0:1], v[0:1], 0, v[62:63]
	v_lshl_add_u64 v[0:1], v[0:1], 3, s[0:1]
	s_waitcnt lgkmcnt(0)
	v_pk_add_f32 v[2:3], v[2:3], v[6:7]
	global_store_dwordx2 v[0:1], v[2:3], off sc1
